# v2_region
# speedup vs baseline: 1.0238x; 1.0238x over previous
.LBB1_9:
	s_waitcnt lgkmcnt(0)
	v_fma_f32 v2, s18, v1, v127
	v_fma_f32 v3, s22, v1, v128
	v_cndmask_b32_e64 v4, v3, v2, s[4:5]
	v_cndmask_b32_e64 v2, v3, v2, s[6:7]
	v_mul_f32_e32 v8, v2, v142
	v_mul_f32_e32 v2, v2, v143
	v_mul_f32_e32 v5, v4, v140
	v_mul_f32_e32 v4, v4, v141
	v_fract_f32_e32 v2, v2
	v_fract_f32_e32 v4, v4
	v_sin_f32_e32 v10, v2
	v_cos_f32_e32 v2, v2
	v_sin_f32_e32 v7, v4
	v_cos_f32_e32 v4, v4
	v_fma_f32 v1, s26, v1, v129
	v_fract_f32_e32 v5, v5
	v_sin_f32_e32 v6, v5
	v_cos_f32_e32 v5, v5
	v_cndmask_b32_e64 v1, v1, v3, s[2:3]
	v_cvt_pk_bf16_f32 v53, v10, v2
	v_mul_f32_e32 v2, v1, v144
	v_cvt_pk_bf16_f32 v51, v7, v4
	v_fract_f32_e32 v2, v2
	v_mul_f32_e32 v4, v1, v145
	v_sin_f32_e32 v3, v2
	v_cos_f32_e32 v2, v2
	v_fract_f32_e32 v4, v4
	v_cvt_pk_bf16_f32 v50, v6, v5
	v_sin_f32_e32 v5, v4
	v_cos_f32_e32 v4, v4
	v_mul_f32_e32 v6, v1, v146
	v_fract_f32_e32 v6, v6
	v_mul_f32_e32 v1, v1, v147
	v_cos_f32_e32 v7, v6
	v_cvt_pk_bf16_f32 v56, v3, v2
	v_sin_f32_e32 v2, v6
	v_fract_f32_e32 v1, v1
	v_cvt_pk_bf16_f32 v57, v5, v4
	v_cos_f32_e32 v4, v1
	v_sin_f32_e32 v1, v1
	v_cndmask_b32_e64 v3, v7, 0, s[0:1]
	v_cndmask_b32_e64 v2, v2, 1.0, s[0:1]
	v_fract_f32_e32 v8, v8
	v_cvt_pk_bf16_f32 v58, v2, v3
	v_cndmask_b32_e64 v2, v4, 0, s[0:1]
	v_cndmask_b32_e64 v1, v1, 0, s[0:1]
	v_sin_f32_e32 v9, v8
	v_cos_f32_e32 v8, v8
	v_cvt_pk_bf16_f32 v59, v1, v2
	v_fma_f32 v1, s18, v0, v127
	v_fma_f32 v2, s22, v0, v128
	v_cndmask_b32_e64 v3, v2, v1, s[4:5]
	v_cndmask_b32_e64 v1, v2, v1, s[6:7]
	v_mul_f32_e32 v7, v1, v142
	v_mul_f32_e32 v1, v1, v143
	v_mul_f32_e32 v4, v3, v140
	v_mul_f32_e32 v3, v3, v141
	v_fract_f32_e32 v1, v1
	v_cvt_pk_bf16_f32 v52, v9, v8
	v_fract_f32_e32 v3, v3
	v_sin_f32_e32 v9, v1
	v_cos_f32_e32 v1, v1
	v_sin_f32_e32 v6, v3
	v_cos_f32_e32 v3, v3
	v_fma_f32 v0, s26, v0, v129
	v_fract_f32_e32 v4, v4
	v_sin_f32_e32 v5, v4
	v_cos_f32_e32 v4, v4
	v_cndmask_b32_e64 v0, v0, v2, s[2:3]
	v_cvt_pk_bf16_f32 v63, v9, v1
	v_mul_f32_e32 v1, v0, v144
	v_cvt_pk_bf16_f32 v61, v6, v3
	v_fract_f32_e32 v1, v1
	v_mul_f32_e32 v3, v0, v145
	v_sin_f32_e32 v2, v1
	v_cos_f32_e32 v1, v1
	v_fract_f32_e32 v3, v3
	v_cvt_pk_bf16_f32 v60, v5, v4
	v_sin_f32_e32 v4, v3
	v_cos_f32_e32 v3, v3
	v_mul_f32_e32 v5, v0, v146
	v_fract_f32_e32 v5, v5
	v_mul_f32_e32 v0, v0, v147
	v_fract_f32_e32 v7, v7
	v_cos_f32_e32 v6, v5
	v_cvt_pk_bf16_f32 v72, v2, v1
	v_sin_f32_e32 v1, v5
	v_fract_f32_e32 v0, v0
	v_sin_f32_e32 v8, v7
	v_cos_f32_e32 v7, v7
	v_cvt_pk_bf16_f32 v73, v4, v3
	v_cos_f32_e32 v3, v0
	v_cndmask_b32_e64 v2, v6, 0, s[0:1]
	v_cndmask_b32_e64 v1, v1, 1.0, s[0:1]
	v_cvt_pk_bf16_f32 v62, v8, v7
	v_cvt_pk_bf16_f32 v74, v1, v2
	v_sin_f32_e32 v16, v0
	v_cndmask_b32_e64 v17, v3, 0, s[0:1]
	s_waitcnt vmcnt(0)
	s_barrier
	ds_read_b128 v[0:3], v148
	ds_read_b128 v[4:7], v149
	ds_read_b128 v[8:11], v150
	ds_read_b128 v[12:15], v151
	v_cndmask_b32_e64 v16, v16, 0, s[0:1]
	v_cvt_pk_bf16_f32 v75, v16, v17
	s_add_i32 s21, s20, 1
	s_lshl_b32 s24, s20, 15
	ds_read_b128 v[20:23], v152
	s_waitcnt lgkmcnt(4)
	v_mfma_f32_16x16x32_bf16 v[16:19], v[0:3], v[50:53], 0
	s_or_b32 s25, s24, 0x2000
	s_or_b32 s46, s24, 0x4000
	s_or_b32 s47, s24, 0x6000
	v_mfma_f32_16x16x32_bf16 v[0:3], v[0:3], v[60:63], 0
	ds_read_b128 v[28:31], v153
	s_waitcnt lgkmcnt(4)
	v_mfma_f32_16x16x32_bf16 v[24:27], v[4:7], v[50:53], 0
	v_mfma_f32_16x16x32_bf16 v[4:7], v[4:7], v[60:63], 0
	ds_read_b128 v[32:35], v154
	s_waitcnt lgkmcnt(4)
	v_mfma_f32_16x16x32_bf16 v[16:19], v[8:11], v[56:59], v[16:19]
	v_mfma_f32_16x16x32_bf16 v[8:11], v[8:11], v[72:75], v[0:3]
	ds_read_b128 v[36:39], v155
	s_waitcnt lgkmcnt(4)
	v_mfma_f32_16x16x32_bf16 v[24:27], v[12:15], v[56:59], v[24:27]
	v_mfma_f32_16x16x32_bf16 v[12:15], v[12:15], v[72:75], v[4:7]
	ds_read_b128 v[44:47], v156
	s_waitcnt lgkmcnt(4)
	v_mfma_f32_16x16x32_bf16 v[40:43], v[20:23], v[50:53], 0
	v_mfma_f32_16x16x32_bf16 v[20:23], v[20:23], v[60:63], 0
	ds_read_b128 v[64:67], v157
	v_cvt_pk_bf16_f32 v0, v16, v17
	s_waitcnt lgkmcnt(4)
	v_mfma_f32_16x16x32_bf16 v[68:71], v[28:31], v[50:53], 0
	v_cvt_pk_bf16_f32 v1, v18, v19
	v_cvt_pk_bf16_f32 v2, v24, v25
	v_cvt_pk_bf16_f32 v3, v26, v27
	v_mfma_f32_16x16x32_bf16 v[16:19], v[28:31], v[60:63], 0
	v_cvt_pk_bf16_f32 v4, v8, v9
	v_cvt_pk_bf16_f32 v5, v10, v11
	v_cvt_pk_bf16_f32 v6, v12, v13
	v_cvt_pk_bf16_f32 v7, v14, v15
	v_pk_max_i16 v0, v0, 0
	v_pk_max_i16 v1, v1, 0
	v_pk_max_i16 v2, v2, 0
	v_pk_max_i16 v3, v3, 0
	v_pk_max_i16 v4, v4, 0
	v_pk_max_i16 v5, v5, 0
	v_pk_max_i16 v6, v6, 0
	v_pk_max_i16 v7, v7, 0
	s_mov_b32 m0, s28
	ds_read_b128 v[24:27], v158
	buffer_load_dwordx4 v125, s[36:39], s24 offen lds
	s_waitcnt lgkmcnt(4)
	v_mfma_f32_16x16x32_bf16 v[8:11], v[32:35], v[56:59], v[40:43]
	v_mfma_f32_16x16x32_bf16 v[20:23], v[32:35], v[72:75], v[20:23]
	ds_read_b128 v[32:35], v159
	s_waitcnt lgkmcnt(4)
	v_mfma_f32_16x16x32_bf16 v[28:31], v[36:39], v[56:59], v[68:71]
	v_mfma_f32_16x16x32_bf16 v[16:19], v[36:39], v[72:75], v[16:19]
	ds_read_b128 v[40:43], v160
	s_waitcnt lgkmcnt(4)
	v_mfma_f32_16x16x32_bf16 v[36:39], v[44:47], v[50:53], 0
	v_mfma_f32_16x16x32_bf16 v[44:47], v[44:47], v[60:63], 0
	v_cvt_pk_bf16_f32 v8, v8, v9
	ds_read_b128 v[68:71], v161
	v_pk_max_i16 v12, v8, 0
	v_cvt_pk_bf16_f32 v8, v10, v11
	s_waitcnt lgkmcnt(4)
	v_mfma_f32_16x16x32_bf16 v[76:79], v[64:67], v[50:53], 0
	v_pk_max_i16 v13, v8, 0
	v_cvt_pk_bf16_f32 v8, v28, v29
	v_pk_max_i16 v14, v8, 0
	v_mfma_f32_16x16x32_bf16 v[64:67], v[64:67], v[60:63], 0
	v_cvt_pk_bf16_f32 v8, v30, v31
	v_pk_max_i16 v15, v8, 0
	v_cvt_pk_bf16_f32 v8, v20, v21
	v_cvt_pk_bf16_f32 v9, v22, v23
	v_cvt_pk_bf16_f32 v10, v16, v17
	v_cvt_pk_bf16_f32 v11, v18, v19
	v_pk_max_i16 v8, v8, 0
	v_pk_max_i16 v9, v9, 0
	v_pk_max_i16 v10, v10, 0
	v_pk_max_i16 v11, v11, 0
	s_mov_b32 m0, s29
	ds_read_b128 v[28:31], v162
	buffer_load_dwordx4 v125, s[36:39], s25 offen lds
	s_waitcnt lgkmcnt(4)
	v_mfma_f32_16x16x32_bf16 v[16:19], v[24:27], v[56:59], v[36:39]
	v_mfma_f32_16x16x32_bf16 v[20:23], v[24:27], v[72:75], v[44:47]
	s_nop 1
	ds_read_b128 v[36:39], v163
	s_waitcnt lgkmcnt(4)
	v_mfma_f32_16x16x32_bf16 v[24:27], v[32:35], v[56:59], v[76:79]
	v_mfma_f32_16x16x32_bf16 v[32:35], v[32:35], v[72:75], v[64:67]
	s_nop 2
	ds_read_b128 v[64:67], v164
	s_waitcnt lgkmcnt(4)
	v_mfma_f32_16x16x32_bf16 v[44:47], v[40:43], v[50:53], 0
	v_mfma_f32_16x16x32_bf16 v[40:43], v[40:43], v[60:63], 0
	ds_read_b128 v[76:79], v165
	s_waitcnt lgkmcnt(4)
	v_mfma_f32_16x16x32_bf16 v[80:83], v[68:71], v[50:53], 0
	v_cvt_pk_bf16_f32 v16, v16, v17
	v_cvt_pk_bf16_f32 v17, v18, v19
	v_cvt_pk_bf16_f32 v18, v24, v25
	v_mfma_f32_16x16x32_bf16 v[68:71], v[68:71], v[60:63], 0
	v_cvt_pk_bf16_f32 v19, v26, v27
	v_cvt_pk_bf16_f32 v20, v20, v21
	v_cvt_pk_bf16_f32 v21, v22, v23
	v_cvt_pk_bf16_f32 v22, v32, v33
	v_cvt_pk_bf16_f32 v23, v34, v35
	v_pk_max_i16 v16, v16, 0
	v_pk_max_i16 v17, v17, 0
	v_pk_max_i16 v18, v18, 0
	v_pk_max_i16 v19, v19, 0
	v_pk_max_i16 v20, v20, 0
	v_pk_max_i16 v21, v21, 0
	v_pk_max_i16 v22, v22, 0
	v_pk_max_i16 v23, v23, 0
	s_mov_b32 m0, s33
	ds_read_b128 v[32:35], v166
	buffer_load_dwordx4 v125, s[36:39], s46 offen lds
	s_waitcnt lgkmcnt(4)
	v_mfma_f32_16x16x32_bf16 v[24:27], v[28:31], v[56:59], v[44:47]
	v_mfma_f32_16x16x32_bf16 v[28:31], v[28:31], v[72:75], v[40:43]
	s_nop 1
	ds_read_b128 v[44:47], v167
	s_waitcnt lgkmcnt(4)
	v_mfma_f32_16x16x32_bf16 v[40:43], v[36:39], v[56:59], v[80:83]
	v_mfma_f32_16x16x32_bf16 v[36:39], v[36:39], v[72:75], v[68:71]
	s_nop 1
	ds_read_b128 v[80:83], v168
	s_waitcnt lgkmcnt(4)
	v_mfma_f32_16x16x32_bf16 v[68:71], v[64:67], v[50:53], 0
	v_mfma_f32_16x16x32_bf16 v[64:67], v[64:67], v[60:63], 0
	ds_read_b128 v[84:87], v169
	s_waitcnt lgkmcnt(4)
	v_mfma_f32_16x16x32_bf16 v[88:91], v[76:79], v[50:53], 0
	v_cvt_pk_bf16_f32 v24, v24, v25
	v_cvt_pk_bf16_f32 v25, v26, v27
	v_cvt_pk_bf16_f32 v26, v40, v41
	v_mfma_f32_16x16x32_bf16 v[76:79], v[76:79], v[60:63], 0
	v_cvt_pk_bf16_f32 v27, v42, v43
	v_cvt_pk_bf16_f32 v28, v28, v29
	v_cvt_pk_bf16_f32 v29, v30, v31
	v_cvt_pk_bf16_f32 v30, v36, v37
	v_cvt_pk_bf16_f32 v31, v38, v39
	v_pk_max_i16 v24, v24, 0
	v_pk_max_i16 v25, v25, 0
	v_pk_max_i16 v26, v26, 0
	v_pk_max_i16 v27, v27, 0
	v_pk_max_i16 v28, v28, 0
	v_pk_max_i16 v29, v29, 0
	v_pk_max_i16 v30, v30, 0
	v_pk_max_i16 v31, v31, 0
	s_mov_b32 m0, s34
	ds_read_b128 v[40:43], v170
	buffer_load_dwordx4 v125, s[36:39], s47 offen lds
	s_waitcnt lgkmcnt(4)
	v_mfma_f32_16x16x32_bf16 v[36:39], v[32:35], v[56:59], v[68:71]
	v_mfma_f32_16x16x32_bf16 v[64:67], v[32:35], v[72:75], v[64:67]
	s_waitcnt lgkmcnt(3)
	v_mfma_f32_16x16x32_bf16 v[68:71], v[44:47], v[56:59], v[88:91]
	s_nop 2
	ds_read_b128 v[88:91], v171
	v_mfma_f32_16x16x32_bf16 v[44:47], v[44:47], v[72:75], v[76:79]
	s_waitcnt lgkmcnt(3)
	v_mfma_f32_16x16x32_bf16 v[76:79], v[80:83], v[50:53], 0
	ds_read_b128 v[92:95], v172
	v_mfma_f32_16x16x32_bf16 v[80:83], v[80:83], v[60:63], 0
	ds_read_b128 v[96:99], v173
	v_cvt_pk_bf16_f32 v32, v36, v37
	v_cvt_pk_bf16_f32 v33, v38, v39
	v_cvt_pk_bf16_f32 v34, v68, v69
	v_cvt_pk_bf16_f32 v35, v70, v71
	v_cvt_pk_bf16_f32 v36, v64, v65
	v_cvt_pk_bf16_f32 v37, v66, v67
	v_cvt_pk_bf16_f32 v38, v44, v45
	v_cvt_pk_bf16_f32 v39, v46, v47
	v_pk_max_i16 v32, v32, 0
	v_pk_max_i16 v33, v33, 0
	v_pk_max_i16 v34, v34, 0
	v_pk_max_i16 v35, v35, 0
	v_pk_max_i16 v36, v36, 0
	v_pk_max_i16 v37, v37, 0
	v_pk_max_i16 v38, v38, 0
	v_pk_max_i16 v39, v39, 0
	s_waitcnt lgkmcnt(4)
	v_mfma_f32_16x16x32_bf16 v[100:103], v[84:87], v[50:53], 0
	v_mfma_f32_16x16x32_bf16 v[84:87], v[84:87], v[60:63], 0
	ds_read_b128 v[64:67], v174
	s_waitcnt lgkmcnt(4)
	v_mfma_f32_16x16x32_bf16 v[44:47], v[40:43], v[56:59], v[76:79]
	v_mfma_f32_16x16x32_bf16 v[68:71], v[40:43], v[72:75], v[80:83]
	s_nop 2
	ds_read_b128 v[80:83], v175
	s_waitcnt lgkmcnt(4)
	v_mfma_f32_16x16x32_bf16 v[76:79], v[88:91], v[56:59], v[100:103]
	v_mfma_f32_16x16x32_bf16 v[84:87], v[88:91], v[72:75], v[84:87]
	s_nop 1
	ds_read_b128 v[100:103], v176
	s_waitcnt lgkmcnt(4)
	v_mfma_f32_16x16x32_bf16 v[88:91], v[92:95], v[50:53], 0
	v_mfma_f32_16x16x32_bf16 v[92:95], v[92:95], v[60:63], 0
	ds_read_b128 v[104:107], v177
	v_cvt_pk_bf16_f32 v40, v44, v45
	v_cvt_pk_bf16_f32 v41, v46, v47
	v_cvt_pk_bf16_f32 v42, v76, v77
	v_cvt_pk_bf16_f32 v43, v78, v79
	v_cvt_pk_bf16_f32 v44, v68, v69
	v_cvt_pk_bf16_f32 v45, v70, v71
	v_cvt_pk_bf16_f32 v46, v84, v85
	v_cvt_pk_bf16_f32 v47, v86, v87
	v_pk_max_i16 v40, v40, 0
	v_pk_max_i16 v41, v41, 0
	v_pk_max_i16 v42, v42, 0
	v_pk_max_i16 v43, v43, 0
	v_pk_max_i16 v44, v44, 0
	v_pk_max_i16 v45, v45, 0
	v_pk_max_i16 v46, v46, 0
	v_pk_max_i16 v47, v47, 0
	s_waitcnt lgkmcnt(4)
	v_mfma_f32_16x16x32_bf16 v[108:111], v[96:99], v[50:53], 0
	v_mfma_f32_16x16x32_bf16 v[96:99], v[96:99], v[60:63], 0
	ds_read_b128 v[76:79], v178
	s_waitcnt lgkmcnt(4)
	v_mfma_f32_16x16x32_bf16 v[68:71], v[64:67], v[56:59], v[88:91]
	v_mfma_f32_16x16x32_bf16 v[64:67], v[64:67], v[72:75], v[92:95]
	s_waitcnt lgkmcnt(3)
	v_mfma_f32_16x16x32_bf16 v[84:87], v[80:83], v[56:59], v[108:111]
	ds_read_b128 v[88:91], v179
	v_mfma_f32_16x16x32_bf16 v[80:83], v[80:83], v[72:75], v[96:99]
	s_waitcnt lgkmcnt(3)
	v_mfma_f32_16x16x32_bf16 v[92:95], v[100:103], v[50:53], 0
	v_mfma_f32_16x16x32_bf16 v[96:99], v[100:103], v[60:63], 0
	v_cvt_pk_bf16_f32 v48, v68, v69
	s_waitcnt lgkmcnt(2)
	v_mfma_f32_16x16x32_bf16 v[100:103], v[104:107], v[50:53], 0
	v_cvt_pk_bf16_f32 v49, v70, v71
	v_cvt_pk_bf16_f32 v50, v84, v85
	v_cvt_pk_bf16_f32 v51, v86, v87
	v_cvt_pk_bf16_f32 v52, v64, v65
	v_cvt_pk_bf16_f32 v53, v66, v67
	v_cvt_pk_bf16_f32 v54, v80, v81
	v_cvt_pk_bf16_f32 v55, v82, v83
	v_pk_max_i16 v48, v48, 0
	v_pk_max_i16 v49, v49, 0
	v_pk_max_i16 v50, v50, 0
	v_pk_max_i16 v51, v51, 0
	v_pk_max_i16 v52, v52, 0
	v_pk_max_i16 v53, v53, 0
	v_pk_max_i16 v54, v54, 0
	v_pk_max_i16 v55, v55, 0
	v_mfma_f32_16x16x32_bf16 v[104:107], v[104:107], v[60:63], 0
	ds_read_b128 v[64:67], v131
	ds_read_b128 v[68:71], v131 offset:64
	s_waitcnt lgkmcnt(3)
	v_mfma_f32_16x16x32_bf16 v[80:83], v[76:79], v[56:59], v[92:95]
	v_mfma_f32_16x16x32_bf16 v[60:63], v[76:79], v[72:75], v[96:99]
	s_waitcnt lgkmcnt(2)
	v_mfma_f32_16x16x32_bf16 v[76:79], v[88:91], v[56:59], v[100:103]
	v_mfma_f32_16x16x32_bf16 v[72:75], v[88:91], v[72:75], v[104:107]
	s_cmp_lg_u32 s20, 29
	s_mov_b32 s20, 0
	s_cselect_b32 s21, s21, 0
	s_waitcnt lgkmcnt(0)
	s_nop 7
	v_mov_b32_e32 v84, v60
	v_mov_b32_e32 v85, v61
	v_mov_b32_e32 v86, v62
	v_mov_b32_e32 v87, v63
	v_mov_b32_e32 v56, v64
	v_mov_b32_e32 v57, v65
	v_mov_b32_e32 v58, v66
	v_mov_b32_e32 v59, v67
	v_mov_b32_e32 v60, v68
	v_mov_b32_e32 v61, v69
	v_mov_b32_e32 v62, v70
	v_mov_b32_e32 v63, v71
	v_mov_b32_e32 v183, v131
	s_mov_b32 s50, 0x10000
	s_mov_b32 s52, 0
	s_waitcnt vmcnt(0) lgkmcnt(0)
	s_barrier
	ds_read_b128 v[224:227], v121 offset:40960
	ds_read_b128 v[228:231], v121 offset:41984
	ds_read_b128 v[232:235], v121 offset:43008
	ds_read_b128 v[236:239], v121 offset:44032
	ds_read_b128 v[240:243], v121 offset:45056
	ds_read_b128 v[244:247], v121 offset:46080
	ds_read_b128 v[248:251], v121 offset:47104
	ds_read_b128 v[252:255], v121 offset:48128
	s_waitcnt lgkmcnt(6)
	v_mfma_f32_16x16x32_bf16 v[64:67], v[224:227], v[0:3], v[64:67]
	v_cvt_pk_bf16_f32 v112, v80, v81
	v_mfma_f32_16x16x32_bf16 v[68:71], v[228:231], v[0:3], v[68:71]
	v_cvt_pk_bf16_f32 v113, v82, v83
	v_mfma_f32_16x16x32_bf16 v[60:63], v[228:231], v[4:7], v[60:63]
	v_cvt_pk_bf16_f32 v114, v76, v77
	v_mfma_f32_16x16x32_bf16 v[56:59], v[224:227], v[4:7], v[56:59]
	v_cvt_pk_bf16_f32 v115, v78, v79
	ds_read_b128 v[224:227], v121 offset:49152
	ds_read_b128 v[228:231], v121 offset:50176
	s_waitcnt lgkmcnt(6)
	v_mfma_f32_16x16x32_bf16 v[64:67], v[232:235], v[12:15], v[64:67]
	v_cvt_pk_bf16_f32 v116, v84, v85
	v_mfma_f32_16x16x32_bf16 v[68:71], v[236:239], v[12:15], v[68:71]
	s_mov_b32 m0, s35
	s_add_i32 s51, s50, 0x0
	v_cvt_pk_bf16_f32 v117, v86, v87
	v_mfma_f32_16x16x32_bf16 v[60:63], v[236:239], v[8:11], v[60:63]
	buffer_load_dwordx4 v125, s[36:39], s51 offen lds
	v_cvt_pk_bf16_f32 v118, v72, v73
	v_mfma_f32_16x16x32_bf16 v[56:59], v[232:235], v[8:11], v[56:59]
	v_cvt_pk_bf16_f32 v119, v74, v75
	ds_read_b128 v[232:235], v121 offset:51200
	ds_read_b128 v[236:239], v121 offset:52224
	s_waitcnt lgkmcnt(6)
	v_mfma_f32_16x16x32_bf16 v[64:67], v[240:243], v[16:19], v[64:67]
	v_pk_max_i16 v112, v112, 0
	v_mfma_f32_16x16x32_bf16 v[68:71], v[244:247], v[16:19], v[68:71]
	s_mov_b32 m0, s42
	s_add_i32 s51, s50, 0x2000
	v_pk_max_i16 v113, v113, 0
	v_mfma_f32_16x16x32_bf16 v[60:63], v[244:247], v[20:23], v[60:63]
	buffer_load_dwordx4 v125, s[36:39], s51 offen lds
	v_pk_max_i16 v114, v114, 0
	v_mfma_f32_16x16x32_bf16 v[56:59], v[240:243], v[20:23], v[56:59]
	v_pk_max_i16 v115, v115, 0
	ds_read_b128 v[240:243], v121 offset:53248
	ds_read_b128 v[244:247], v121 offset:54272
	s_waitcnt lgkmcnt(6)
	v_mfma_f32_16x16x32_bf16 v[64:67], v[248:251], v[24:27], v[64:67]
	v_pk_max_i16 v116, v116, 0
	v_mfma_f32_16x16x32_bf16 v[68:71], v[252:255], v[24:27], v[68:71]
	s_mov_b32 m0, s41
	s_add_i32 s51, s50, 0x4000
	v_pk_max_i16 v117, v117, 0
	v_mfma_f32_16x16x32_bf16 v[60:63], v[252:255], v[28:31], v[60:63]
	buffer_load_dwordx4 v125, s[36:39], s51 offen lds
	v_pk_max_i16 v118, v118, 0
	v_mfma_f32_16x16x32_bf16 v[56:59], v[248:251], v[28:31], v[56:59]
	v_pk_max_i16 v119, v119, 0
	ds_read_b128 v[248:251], v121 offset:55296
	ds_read_b128 v[252:255], v121 offset:56320
	s_waitcnt lgkmcnt(6)
	v_mfma_f32_16x16x32_bf16 v[64:67], v[224:227], v[32:35], v[64:67]
	ds_read_b128 v[80:83], v183 offset:128
	ds_read_b128 v[84:87], v183 offset:128
	ds_read_b128 v[76:79], v183 offset:192
	ds_read_b128 v[72:75], v183 offset:192
	v_mfma_f32_16x16x32_bf16 v[68:71], v[228:231], v[32:35], v[68:71]
	s_mov_b32 m0, s40
	s_add_i32 s51, s50, 0x6000
	v_mfma_f32_16x16x32_bf16 v[60:63], v[228:231], v[36:39], v[60:63]
	buffer_load_dwordx4 v125, s[36:39], s51 offen lds
	v_mfma_f32_16x16x32_bf16 v[56:59], v[224:227], v[36:39], v[56:59]
	ds_read_b128 v[224:227], v121 offset:57344
	ds_read_b128 v[228:231], v121 offset:58368
	s_waitcnt lgkmcnt(10)
	v_mfma_f32_16x16x32_bf16 v[64:67], v[232:235], v[40:43], v[64:67]
	v_mfma_f32_16x16x32_bf16 v[68:71], v[236:239], v[40:43], v[68:71]
	v_mfma_f32_16x16x32_bf16 v[60:63], v[236:239], v[44:47], v[60:63]
	v_mfma_f32_16x16x32_bf16 v[56:59], v[232:235], v[44:47], v[56:59]
	ds_read_b128 v[232:235], v121 offset:59392
	ds_read_b128 v[236:239], v121 offset:60416
	s_waitcnt lgkmcnt(10)
	v_mfma_f32_16x16x32_bf16 v[64:67], v[240:243], v[48:51], v[64:67]
	v_mfma_f32_16x16x32_bf16 v[68:71], v[244:247], v[48:51], v[68:71]
	v_mfma_f32_16x16x32_bf16 v[60:63], v[244:247], v[52:55], v[60:63]
	v_mfma_f32_16x16x32_bf16 v[56:59], v[240:243], v[52:55], v[56:59]
	ds_read_b128 v[240:243], v121 offset:61440
	ds_read_b128 v[244:247], v121 offset:62464
	s_waitcnt lgkmcnt(10)
	v_mfma_f32_16x16x32_bf16 v[64:67], v[248:251], v[112:115], v[64:67]
	v_mfma_f32_16x16x32_bf16 v[68:71], v[252:255], v[112:115], v[68:71]
	v_mfma_f32_16x16x32_bf16 v[60:63], v[252:255], v[116:119], v[60:63]
	v_mfma_f32_16x16x32_bf16 v[56:59], v[248:251], v[116:119], v[56:59]
	ds_read_b128 v[248:251], v121 offset:63488
	ds_read_b128 v[252:255], v121 offset:64512
	s_waitcnt lgkmcnt(6)
	v_mfma_f32_16x16x32_bf16 v[80:83], v[224:227], v[0:3], v[80:83]
	v_mfma_f32_16x16x32_bf16 v[76:79], v[228:231], v[0:3], v[76:79]
	v_mfma_f32_16x16x32_bf16 v[72:75], v[228:231], v[4:7], v[72:75]
	v_mfma_f32_16x16x32_bf16 v[84:87], v[224:227], v[4:7], v[84:87]
	ds_read_b128 v[224:227], v126 offset:57344
	ds_read_b128 v[228:231], v126 offset:58368
	s_waitcnt lgkmcnt(6)
	v_mfma_f32_16x16x32_bf16 v[80:83], v[232:235], v[12:15], v[80:83]
	v_cvt_pk_bf16_f32 v88, v64, v65
	v_mfma_f32_16x16x32_bf16 v[76:79], v[236:239], v[12:15], v[76:79]
	v_cvt_pk_bf16_f32 v89, v66, v67
	v_mfma_f32_16x16x32_bf16 v[72:75], v[236:239], v[8:11], v[72:75]
	v_cvt_pk_bf16_f32 v90, v68, v69
	v_mfma_f32_16x16x32_bf16 v[84:87], v[232:235], v[8:11], v[84:87]
	v_cvt_pk_bf16_f32 v91, v70, v71
	ds_read_b128 v[232:235], v126 offset:59392
	ds_read_b128 v[236:239], v126 offset:60416
	s_waitcnt lgkmcnt(6)
	v_mfma_f32_16x16x32_bf16 v[80:83], v[240:243], v[16:19], v[80:83]
	v_cvt_pk_bf16_f32 v92, v56, v57
	v_mfma_f32_16x16x32_bf16 v[76:79], v[244:247], v[16:19], v[76:79]
	v_cvt_pk_bf16_f32 v93, v58, v59
	v_mfma_f32_16x16x32_bf16 v[72:75], v[244:247], v[20:23], v[72:75]
	v_cvt_pk_bf16_f32 v94, v60, v61
	v_mfma_f32_16x16x32_bf16 v[84:87], v[240:243], v[20:23], v[84:87]
	v_cvt_pk_bf16_f32 v95, v62, v63
	ds_read_b128 v[240:243], v126 offset:61440
	ds_read_b128 v[244:247], v126 offset:62464
	s_waitcnt lgkmcnt(6)
	v_mfma_f32_16x16x32_bf16 v[80:83], v[248:251], v[24:27], v[80:83]
	v_pk_max_i16 v88, v88, 0
	v_mfma_f32_16x16x32_bf16 v[76:79], v[252:255], v[24:27], v[76:79]
	v_pk_max_i16 v89, v89, 0
	v_mfma_f32_16x16x32_bf16 v[72:75], v[252:255], v[28:31], v[72:75]
	v_pk_max_i16 v90, v90, 0
	v_mfma_f32_16x16x32_bf16 v[84:87], v[248:251], v[28:31], v[84:87]
	v_pk_max_i16 v91, v91, 0
	ds_read_b128 v[248:251], v126 offset:63488
	ds_read_b128 v[252:255], v126 offset:64512
	s_waitcnt lgkmcnt(6)
	v_mfma_f32_16x16x32_bf16 v[80:83], v[224:227], v[32:35], v[80:83]
	v_pk_max_i16 v92, v92, 0
	v_mfma_f32_16x16x32_bf16 v[76:79], v[228:231], v[32:35], v[76:79]
	v_pk_max_i16 v93, v93, 0
	v_mfma_f32_16x16x32_bf16 v[72:75], v[228:231], v[36:39], v[72:75]
	v_pk_max_i16 v94, v94, 0
	v_mfma_f32_16x16x32_bf16 v[84:87], v[224:227], v[36:39], v[84:87]
	v_pk_max_i16 v95, v95, 0
	s_waitcnt lgkmcnt(4)
	v_mfma_f32_16x16x32_bf16 v[80:83], v[232:235], v[40:43], v[80:83]
	ds_read_b128 v[64:67], v183 offset:256
	ds_read_b128 v[56:59], v183 offset:256
	ds_read_b128 v[68:71], v183 offset:320
	ds_read_b128 v[60:63], v183 offset:320
	v_mfma_f32_16x16x32_bf16 v[76:79], v[236:239], v[40:43], v[76:79]
	v_mfma_f32_16x16x32_bf16 v[72:75], v[236:239], v[44:47], v[72:75]
	v_mfma_f32_16x16x32_bf16 v[84:87], v[232:235], v[44:47], v[84:87]
	s_branch .Lnerf_hid_b1
.Lnerf_hid_b0:
	s_waitcnt vmcnt(0) lgkmcnt(0)
	s_barrier
	ds_read_b128 v[224:227], v121 offset:40960
	ds_read_b128 v[228:231], v121 offset:41984
	ds_read_b128 v[232:235], v121 offset:43008
	ds_read_b128 v[236:239], v121 offset:44032
	v_mfma_f32_16x16x32_bf16 v[80:83], v[240:243], v[208:211], v[80:83]
	v_mfma_f32_16x16x32_bf16 v[76:79], v[244:247], v[208:211], v[76:79]
	v_mfma_f32_16x16x32_bf16 v[72:75], v[244:247], v[212:215], v[72:75]
	v_mfma_f32_16x16x32_bf16 v[84:87], v[240:243], v[212:215], v[84:87]
	ds_read_b128 v[240:243], v121 offset:45056
	ds_read_b128 v[244:247], v121 offset:46080
	v_mfma_f32_16x16x32_bf16 v[80:83], v[248:251], v[216:219], v[80:83]
	v_mfma_f32_16x16x32_bf16 v[76:79], v[252:255], v[216:219], v[76:79]
	v_mfma_f32_16x16x32_bf16 v[72:75], v[252:255], v[220:223], v[72:75]
	v_mfma_f32_16x16x32_bf16 v[84:87], v[248:251], v[220:223], v[84:87]
	ds_read_b128 v[248:251], v121 offset:47104
	ds_read_b128 v[252:255], v121 offset:48128
	s_waitcnt lgkmcnt(6)
	v_mfma_f32_16x16x32_bf16 v[64:67], v[224:227], v[0:3], v[64:67]
	v_mfma_f32_16x16x32_bf16 v[68:71], v[228:231], v[0:3], v[68:71]
	v_mfma_f32_16x16x32_bf16 v[60:63], v[228:231], v[4:7], v[60:63]
	v_mfma_f32_16x16x32_bf16 v[56:59], v[224:227], v[4:7], v[56:59]
	ds_read_b128 v[224:227], v121 offset:49152
	ds_read_b128 v[228:231], v121 offset:50176
	s_waitcnt lgkmcnt(6)
	v_mfma_f32_16x16x32_bf16 v[64:67], v[232:235], v[12:15], v[64:67]
	v_cvt_pk_bf16_f32 v112, v80, v81
	v_mfma_f32_16x16x32_bf16 v[68:71], v[236:239], v[12:15], v[68:71]
	s_mov_b32 m0, s35
	s_add_i32 s51, s50, 0x0
	v_cvt_pk_bf16_f32 v113, v82, v83
	v_mfma_f32_16x16x32_bf16 v[60:63], v[236:239], v[8:11], v[60:63]
	buffer_load_dwordx4 v125, s[36:39], s51 offen lds
	v_cvt_pk_bf16_f32 v114, v76, v77
	v_mfma_f32_16x16x32_bf16 v[56:59], v[232:235], v[8:11], v[56:59]
	v_cvt_pk_bf16_f32 v115, v78, v79
	ds_read_b128 v[232:235], v121 offset:51200
	ds_read_b128 v[236:239], v121 offset:52224
	s_waitcnt lgkmcnt(6)
	v_mfma_f32_16x16x32_bf16 v[64:67], v[240:243], v[16:19], v[64:67]
	v_cvt_pk_bf16_f32 v116, v84, v85
	v_mfma_f32_16x16x32_bf16 v[68:71], v[244:247], v[16:19], v[68:71]
	s_mov_b32 m0, s42
	s_add_i32 s51, s50, 0x2000
	v_cvt_pk_bf16_f32 v117, v86, v87
	v_mfma_f32_16x16x32_bf16 v[60:63], v[244:247], v[20:23], v[60:63]
	buffer_load_dwordx4 v125, s[36:39], s51 offen lds
	v_cvt_pk_bf16_f32 v118, v72, v73
	v_mfma_f32_16x16x32_bf16 v[56:59], v[240:243], v[20:23], v[56:59]
	v_cvt_pk_bf16_f32 v119, v74, v75
	ds_read_b128 v[240:243], v121 offset:53248
	ds_read_b128 v[244:247], v121 offset:54272
	s_waitcnt lgkmcnt(6)
	v_mfma_f32_16x16x32_bf16 v[64:67], v[248:251], v[24:27], v[64:67]
	v_pk_max_i16 v112, v112, 0
	v_mfma_f32_16x16x32_bf16 v[68:71], v[252:255], v[24:27], v[68:71]
	s_mov_b32 m0, s41
	s_add_i32 s51, s50, 0x4000
	v_pk_max_i16 v113, v113, 0
	v_mfma_f32_16x16x32_bf16 v[60:63], v[252:255], v[28:31], v[60:63]
	buffer_load_dwordx4 v125, s[36:39], s51 offen lds
	v_pk_max_i16 v114, v114, 0
	v_mfma_f32_16x16x32_bf16 v[56:59], v[248:251], v[28:31], v[56:59]
	v_pk_max_i16 v115, v115, 0
	ds_read_b128 v[248:251], v121 offset:55296
	ds_read_b128 v[252:255], v121 offset:56320
	s_waitcnt lgkmcnt(6)
	v_mfma_f32_16x16x32_bf16 v[64:67], v[224:227], v[32:35], v[64:67]
	v_pk_max_i16 v116, v116, 0
	v_mfma_f32_16x16x32_bf16 v[68:71], v[228:231], v[32:35], v[68:71]
	s_mov_b32 m0, s40
	s_add_i32 s51, s50, 0x6000
	v_pk_max_i16 v117, v117, 0
	v_mfma_f32_16x16x32_bf16 v[60:63], v[228:231], v[36:39], v[60:63]
	buffer_load_dwordx4 v125, s[36:39], s51 offen lds
	v_pk_max_i16 v118, v118, 0
	v_mfma_f32_16x16x32_bf16 v[56:59], v[224:227], v[36:39], v[56:59]
	v_pk_max_i16 v119, v119, 0
	ds_read_b128 v[224:227], v121 offset:57344
	ds_read_b128 v[228:231], v121 offset:58368
	s_waitcnt lgkmcnt(6)
	v_mfma_f32_16x16x32_bf16 v[64:67], v[232:235], v[40:43], v[64:67]
	ds_read_b128 v[80:83], v183 offset:128
	ds_read_b128 v[84:87], v183 offset:128
	ds_read_b128 v[76:79], v183 offset:192
	ds_read_b128 v[72:75], v183 offset:192
	v_mfma_f32_16x16x32_bf16 v[68:71], v[236:239], v[40:43], v[68:71]
	v_mfma_f32_16x16x32_bf16 v[60:63], v[236:239], v[44:47], v[60:63]
	v_mfma_f32_16x16x32_bf16 v[56:59], v[232:235], v[44:47], v[56:59]
	ds_read_b128 v[232:235], v121 offset:59392
	ds_read_b128 v[236:239], v121 offset:60416
	s_waitcnt lgkmcnt(10)
	v_mfma_f32_16x16x32_bf16 v[64:67], v[240:243], v[48:51], v[64:67]
	v_mfma_f32_16x16x32_bf16 v[68:71], v[244:247], v[48:51], v[68:71]
	v_mfma_f32_16x16x32_bf16 v[60:63], v[244:247], v[52:55], v[60:63]
	v_mfma_f32_16x16x32_bf16 v[56:59], v[240:243], v[52:55], v[56:59]
	ds_read_b128 v[240:243], v121 offset:61440
	ds_read_b128 v[244:247], v121 offset:62464
	s_waitcnt lgkmcnt(10)
	v_mfma_f32_16x16x32_bf16 v[64:67], v[248:251], v[112:115], v[64:67]
	v_mfma_f32_16x16x32_bf16 v[68:71], v[252:255], v[112:115], v[68:71]
	v_mfma_f32_16x16x32_bf16 v[60:63], v[252:255], v[116:119], v[60:63]
	v_mfma_f32_16x16x32_bf16 v[56:59], v[248:251], v[116:119], v[56:59]
	ds_read_b128 v[248:251], v121 offset:63488
	ds_read_b128 v[252:255], v121 offset:64512
	s_waitcnt lgkmcnt(6)
	v_mfma_f32_16x16x32_bf16 v[80:83], v[224:227], v[0:3], v[80:83]
	v_mfma_f32_16x16x32_bf16 v[76:79], v[228:231], v[0:3], v[76:79]
	v_mfma_f32_16x16x32_bf16 v[72:75], v[228:231], v[4:7], v[72:75]
	v_mfma_f32_16x16x32_bf16 v[84:87], v[224:227], v[4:7], v[84:87]
	ds_read_b128 v[224:227], v126 offset:57344
	ds_read_b128 v[228:231], v126 offset:58368
	s_waitcnt lgkmcnt(6)
	v_mfma_f32_16x16x32_bf16 v[80:83], v[232:235], v[12:15], v[80:83]
	v_cvt_pk_bf16_f32 v88, v64, v65
	v_mfma_f32_16x16x32_bf16 v[76:79], v[236:239], v[12:15], v[76:79]
	v_cvt_pk_bf16_f32 v89, v66, v67
	v_mfma_f32_16x16x32_bf16 v[72:75], v[236:239], v[8:11], v[72:75]
	v_cvt_pk_bf16_f32 v90, v68, v69
	v_mfma_f32_16x16x32_bf16 v[84:87], v[232:235], v[8:11], v[84:87]
	v_cvt_pk_bf16_f32 v91, v70, v71
	ds_read_b128 v[232:235], v126 offset:59392
	ds_read_b128 v[236:239], v126 offset:60416
	s_waitcnt lgkmcnt(6)
	v_mfma_f32_16x16x32_bf16 v[80:83], v[240:243], v[16:19], v[80:83]
	v_cvt_pk_bf16_f32 v92, v56, v57
	v_mfma_f32_16x16x32_bf16 v[76:79], v[244:247], v[16:19], v[76:79]
	v_cvt_pk_bf16_f32 v93, v58, v59
	v_mfma_f32_16x16x32_bf16 v[72:75], v[244:247], v[20:23], v[72:75]
	v_cvt_pk_bf16_f32 v94, v60, v61
	v_mfma_f32_16x16x32_bf16 v[84:87], v[240:243], v[20:23], v[84:87]
	v_cvt_pk_bf16_f32 v95, v62, v63
	ds_read_b128 v[240:243], v126 offset:61440
	ds_read_b128 v[244:247], v126 offset:62464
	s_waitcnt lgkmcnt(6)
	v_mfma_f32_16x16x32_bf16 v[80:83], v[248:251], v[24:27], v[80:83]
	v_pk_max_i16 v88, v88, 0
	v_mfma_f32_16x16x32_bf16 v[76:79], v[252:255], v[24:27], v[76:79]
	v_pk_max_i16 v89, v89, 0
	v_mfma_f32_16x16x32_bf16 v[72:75], v[252:255], v[28:31], v[72:75]
	v_pk_max_i16 v90, v90, 0
	v_mfma_f32_16x16x32_bf16 v[84:87], v[248:251], v[28:31], v[84:87]
	v_pk_max_i16 v91, v91, 0
	ds_read_b128 v[248:251], v126 offset:63488
	ds_read_b128 v[252:255], v126 offset:64512
	s_waitcnt lgkmcnt(6)
	v_mfma_f32_16x16x32_bf16 v[80:83], v[224:227], v[32:35], v[80:83]
	v_pk_max_i16 v92, v92, 0
	v_mfma_f32_16x16x32_bf16 v[76:79], v[228:231], v[32:35], v[76:79]
	v_pk_max_i16 v93, v93, 0
	v_mfma_f32_16x16x32_bf16 v[72:75], v[228:231], v[36:39], v[72:75]
	v_pk_max_i16 v94, v94, 0
	v_mfma_f32_16x16x32_bf16 v[84:87], v[224:227], v[36:39], v[84:87]
	v_pk_max_i16 v95, v95, 0
	s_waitcnt lgkmcnt(4)
	v_mfma_f32_16x16x32_bf16 v[80:83], v[232:235], v[40:43], v[80:83]
	ds_read_b128 v[64:67], v183 offset:256
	ds_read_b128 v[56:59], v183 offset:256
	ds_read_b128 v[68:71], v183 offset:320
	ds_read_b128 v[60:63], v183 offset:320
	v_mfma_f32_16x16x32_bf16 v[76:79], v[236:239], v[40:43], v[76:79]
	v_mfma_f32_16x16x32_bf16 v[72:75], v[236:239], v[44:47], v[72:75]
	v_mfma_f32_16x16x32_bf16 v[84:87], v[232:235], v[44:47], v[84:87]
.Lnerf_hid_b1:
	s_waitcnt vmcnt(0) lgkmcnt(0)
	s_barrier
	ds_read_b128 v[224:227], v121 offset:8192
	ds_read_b128 v[228:231], v121 offset:9216
	ds_read_b128 v[232:235], v121 offset:10240
	ds_read_b128 v[236:239], v121 offset:11264
	v_mfma_f32_16x16x32_bf16 v[80:83], v[240:243], v[48:51], v[80:83]
	v_mfma_f32_16x16x32_bf16 v[76:79], v[244:247], v[48:51], v[76:79]
	v_mfma_f32_16x16x32_bf16 v[72:75], v[244:247], v[52:55], v[72:75]
	v_mfma_f32_16x16x32_bf16 v[84:87], v[240:243], v[52:55], v[84:87]
	ds_read_b128 v[240:243], v121 offset:12288
	ds_read_b128 v[244:247], v121 offset:13312
	v_mfma_f32_16x16x32_bf16 v[80:83], v[248:251], v[112:115], v[80:83]
	v_mfma_f32_16x16x32_bf16 v[76:79], v[252:255], v[112:115], v[76:79]
	v_mfma_f32_16x16x32_bf16 v[72:75], v[252:255], v[116:119], v[72:75]
	v_mfma_f32_16x16x32_bf16 v[84:87], v[248:251], v[116:119], v[84:87]
	ds_read_b128 v[248:251], v121 offset:14336
	ds_read_b128 v[252:255], v121 offset:15360
	s_waitcnt lgkmcnt(6)
	v_mfma_f32_16x16x32_bf16 v[64:67], v[224:227], v[0:3], v[64:67]
	v_mfma_f32_16x16x32_bf16 v[68:71], v[228:231], v[0:3], v[68:71]
	v_mfma_f32_16x16x32_bf16 v[60:63], v[228:231], v[4:7], v[60:63]
	v_mfma_f32_16x16x32_bf16 v[56:59], v[224:227], v[4:7], v[56:59]
	ds_read_b128 v[224:227], v121 offset:16384
	ds_read_b128 v[228:231], v121 offset:17408
	s_waitcnt lgkmcnt(6)
	v_mfma_f32_16x16x32_bf16 v[64:67], v[232:235], v[12:15], v[64:67]
	v_cvt_pk_bf16_f32 v96, v80, v81
	v_mfma_f32_16x16x32_bf16 v[68:71], v[236:239], v[12:15], v[68:71]
	s_mov_b32 m0, s28
	s_add_i32 s51, s50, 0x8000
	v_cvt_pk_bf16_f32 v97, v82, v83
	v_mfma_f32_16x16x32_bf16 v[60:63], v[236:239], v[8:11], v[60:63]
	buffer_load_dwordx4 v125, s[36:39], s51 offen lds
	v_cvt_pk_bf16_f32 v98, v76, v77
	v_mfma_f32_16x16x32_bf16 v[56:59], v[232:235], v[8:11], v[56:59]
	v_cvt_pk_bf16_f32 v99, v78, v79
	ds_read_b128 v[232:235], v121 offset:18432
	ds_read_b128 v[236:239], v121 offset:19456
	s_waitcnt lgkmcnt(6)
	v_mfma_f32_16x16x32_bf16 v[64:67], v[240:243], v[16:19], v[64:67]
	v_cvt_pk_bf16_f32 v100, v84, v85
	v_mfma_f32_16x16x32_bf16 v[68:71], v[244:247], v[16:19], v[68:71]
	s_mov_b32 m0, s29
	s_add_i32 s51, s50, 0xa000
	v_cvt_pk_bf16_f32 v101, v86, v87
	v_mfma_f32_16x16x32_bf16 v[60:63], v[244:247], v[20:23], v[60:63]
	buffer_load_dwordx4 v125, s[36:39], s51 offen lds
	v_cvt_pk_bf16_f32 v102, v72, v73
	v_mfma_f32_16x16x32_bf16 v[56:59], v[240:243], v[20:23], v[56:59]
	v_cvt_pk_bf16_f32 v103, v74, v75
	ds_read_b128 v[240:243], v121 offset:20480
	ds_read_b128 v[244:247], v121 offset:21504
	s_waitcnt lgkmcnt(6)
	v_mfma_f32_16x16x32_bf16 v[64:67], v[248:251], v[24:27], v[64:67]
	v_pk_max_i16 v96, v96, 0
	v_mfma_f32_16x16x32_bf16 v[68:71], v[252:255], v[24:27], v[68:71]
	s_mov_b32 m0, s33
	s_add_i32 s51, s50, 0xc000
	v_pk_max_i16 v97, v97, 0
	v_mfma_f32_16x16x32_bf16 v[60:63], v[252:255], v[28:31], v[60:63]
	buffer_load_dwordx4 v125, s[36:39], s51 offen lds
	v_pk_max_i16 v98, v98, 0
	v_mfma_f32_16x16x32_bf16 v[56:59], v[248:251], v[28:31], v[56:59]
	v_pk_max_i16 v99, v99, 0
	ds_read_b128 v[248:251], v121 offset:22528
	ds_read_b128 v[252:255], v121 offset:23552
	s_waitcnt lgkmcnt(6)
	v_mfma_f32_16x16x32_bf16 v[64:67], v[224:227], v[32:35], v[64:67]
	v_pk_max_i16 v100, v100, 0
	v_mfma_f32_16x16x32_bf16 v[68:71], v[228:231], v[32:35], v[68:71]
	s_mov_b32 m0, s34
	s_add_i32 s51, s50, 0xe000
	v_pk_max_i16 v101, v101, 0
	v_mfma_f32_16x16x32_bf16 v[60:63], v[228:231], v[36:39], v[60:63]
	buffer_load_dwordx4 v125, s[36:39], s51 offen lds
	v_pk_max_i16 v102, v102, 0
	v_mfma_f32_16x16x32_bf16 v[56:59], v[224:227], v[36:39], v[56:59]
	v_pk_max_i16 v103, v103, 0
	ds_read_b128 v[224:227], v121 offset:24576
	ds_read_b128 v[228:231], v121 offset:25600
	s_waitcnt lgkmcnt(6)
	v_mfma_f32_16x16x32_bf16 v[64:67], v[232:235], v[40:43], v[64:67]
	ds_read_b128 v[80:83], v183 offset:384
	ds_read_b128 v[84:87], v183 offset:384
	ds_read_b128 v[76:79], v183 offset:448
	ds_read_b128 v[72:75], v183 offset:448
	v_mfma_f32_16x16x32_bf16 v[68:71], v[236:239], v[40:43], v[68:71]
	v_mfma_f32_16x16x32_bf16 v[60:63], v[236:239], v[44:47], v[60:63]
	v_mfma_f32_16x16x32_bf16 v[56:59], v[232:235], v[44:47], v[56:59]
	ds_read_b128 v[232:235], v121 offset:26624
	ds_read_b128 v[236:239], v121 offset:27648
	s_waitcnt lgkmcnt(10)
	v_mfma_f32_16x16x32_bf16 v[64:67], v[240:243], v[48:51], v[64:67]
	v_mfma_f32_16x16x32_bf16 v[68:71], v[244:247], v[48:51], v[68:71]
	v_mfma_f32_16x16x32_bf16 v[60:63], v[244:247], v[52:55], v[60:63]
	v_mfma_f32_16x16x32_bf16 v[56:59], v[240:243], v[52:55], v[56:59]
	ds_read_b128 v[240:243], v121 offset:28672
	ds_read_b128 v[244:247], v121 offset:29696
	s_waitcnt lgkmcnt(10)
	v_mfma_f32_16x16x32_bf16 v[64:67], v[248:251], v[112:115], v[64:67]
	v_mfma_f32_16x16x32_bf16 v[68:71], v[252:255], v[112:115], v[68:71]
	v_mfma_f32_16x16x32_bf16 v[60:63], v[252:255], v[116:119], v[60:63]
	v_mfma_f32_16x16x32_bf16 v[56:59], v[248:251], v[116:119], v[56:59]
	ds_read_b128 v[248:251], v121 offset:30720
	ds_read_b128 v[252:255], v121 offset:31744
	s_waitcnt lgkmcnt(6)
	v_mfma_f32_16x16x32_bf16 v[80:83], v[224:227], v[0:3], v[80:83]
	v_mfma_f32_16x16x32_bf16 v[76:79], v[228:231], v[0:3], v[76:79]
	v_mfma_f32_16x16x32_bf16 v[72:75], v[228:231], v[4:7], v[72:75]
	v_mfma_f32_16x16x32_bf16 v[84:87], v[224:227], v[4:7], v[84:87]
	ds_read_b128 v[224:227], v121 offset:32768
	ds_read_b128 v[228:231], v121 offset:33792
	s_waitcnt lgkmcnt(6)
	v_mfma_f32_16x16x32_bf16 v[80:83], v[232:235], v[12:15], v[80:83]
	v_cvt_pk_bf16_f32 v104, v64, v65
	v_mfma_f32_16x16x32_bf16 v[76:79], v[236:239], v[12:15], v[76:79]
	v_cvt_pk_bf16_f32 v105, v66, v67
	v_mfma_f32_16x16x32_bf16 v[72:75], v[236:239], v[8:11], v[72:75]
	v_cvt_pk_bf16_f32 v106, v68, v69
	v_mfma_f32_16x16x32_bf16 v[84:87], v[232:235], v[8:11], v[84:87]
	v_cvt_pk_bf16_f32 v107, v70, v71
	ds_read_b128 v[232:235], v121 offset:34816
	ds_read_b128 v[236:239], v121 offset:35840
	s_waitcnt lgkmcnt(6)
	v_mfma_f32_16x16x32_bf16 v[80:83], v[240:243], v[16:19], v[80:83]
	v_cvt_pk_bf16_f32 v108, v56, v57
	v_mfma_f32_16x16x32_bf16 v[76:79], v[244:247], v[16:19], v[76:79]
	v_cvt_pk_bf16_f32 v109, v58, v59
	v_mfma_f32_16x16x32_bf16 v[72:75], v[244:247], v[20:23], v[72:75]
	v_cvt_pk_bf16_f32 v110, v60, v61
	v_mfma_f32_16x16x32_bf16 v[84:87], v[240:243], v[20:23], v[84:87]
	v_cvt_pk_bf16_f32 v111, v62, v63
	ds_read_b128 v[240:243], v121 offset:36864
	ds_read_b128 v[244:247], v121 offset:37888
	s_waitcnt lgkmcnt(6)
	v_mfma_f32_16x16x32_bf16 v[80:83], v[248:251], v[24:27], v[80:83]
	v_pk_max_i16 v104, v104, 0
	v_mfma_f32_16x16x32_bf16 v[76:79], v[252:255], v[24:27], v[76:79]
	v_pk_max_i16 v105, v105, 0
	v_mfma_f32_16x16x32_bf16 v[72:75], v[252:255], v[28:31], v[72:75]
	v_pk_max_i16 v106, v106, 0
	v_mfma_f32_16x16x32_bf16 v[84:87], v[248:251], v[28:31], v[84:87]
	v_pk_max_i16 v107, v107, 0
	ds_read_b128 v[248:251], v121 offset:38912
	ds_read_b128 v[252:255], v121 offset:39936
	s_waitcnt lgkmcnt(6)
	v_mfma_f32_16x16x32_bf16 v[80:83], v[224:227], v[32:35], v[80:83]
	v_pk_max_i16 v108, v108, 0
	v_mfma_f32_16x16x32_bf16 v[76:79], v[228:231], v[32:35], v[76:79]
	v_pk_max_i16 v109, v109, 0
	v_mfma_f32_16x16x32_bf16 v[72:75], v[228:231], v[36:39], v[72:75]
	v_pk_max_i16 v110, v110, 0
	v_mfma_f32_16x16x32_bf16 v[84:87], v[224:227], v[36:39], v[84:87]
	v_pk_max_i16 v111, v111, 0
	s_waitcnt lgkmcnt(4)
	v_mfma_f32_16x16x32_bf16 v[80:83], v[232:235], v[40:43], v[80:83]
	ds_read_b128 v[64:67], v183 offset:512
	ds_read_b128 v[56:59], v183 offset:512
	ds_read_b128 v[68:71], v183 offset:576
	ds_read_b128 v[60:63], v183 offset:576
	v_mfma_f32_16x16x32_bf16 v[76:79], v[236:239], v[40:43], v[76:79]
	v_mfma_f32_16x16x32_bf16 v[72:75], v[236:239], v[44:47], v[72:75]
	v_mfma_f32_16x16x32_bf16 v[84:87], v[232:235], v[44:47], v[84:87]
.Lnerf_hid_b2:
	s_waitcnt vmcnt(0) lgkmcnt(0)
	s_barrier
	ds_read_b128 v[224:227], v121 offset:40960
	ds_read_b128 v[228:231], v121 offset:41984
	ds_read_b128 v[232:235], v121 offset:43008
	ds_read_b128 v[236:239], v121 offset:44032
	v_mfma_f32_16x16x32_bf16 v[80:83], v[240:243], v[48:51], v[80:83]
	v_mfma_f32_16x16x32_bf16 v[76:79], v[244:247], v[48:51], v[76:79]
	v_mfma_f32_16x16x32_bf16 v[72:75], v[244:247], v[52:55], v[72:75]
	v_mfma_f32_16x16x32_bf16 v[84:87], v[240:243], v[52:55], v[84:87]
	ds_read_b128 v[240:243], v121 offset:45056
	ds_read_b128 v[244:247], v121 offset:46080
	v_mfma_f32_16x16x32_bf16 v[80:83], v[248:251], v[112:115], v[80:83]
	v_mfma_f32_16x16x32_bf16 v[76:79], v[252:255], v[112:115], v[76:79]
	v_mfma_f32_16x16x32_bf16 v[72:75], v[252:255], v[116:119], v[72:75]
	v_mfma_f32_16x16x32_bf16 v[84:87], v[248:251], v[116:119], v[84:87]
	ds_read_b128 v[248:251], v121 offset:47104
	ds_read_b128 v[252:255], v121 offset:48128
	s_waitcnt lgkmcnt(6)
	v_mfma_f32_16x16x32_bf16 v[64:67], v[224:227], v[0:3], v[64:67]
	v_mfma_f32_16x16x32_bf16 v[68:71], v[228:231], v[0:3], v[68:71]
	v_mfma_f32_16x16x32_bf16 v[60:63], v[228:231], v[4:7], v[60:63]
	v_mfma_f32_16x16x32_bf16 v[56:59], v[224:227], v[4:7], v[56:59]
	ds_read_b128 v[224:227], v121 offset:49152
	ds_read_b128 v[228:231], v121 offset:50176
	s_waitcnt lgkmcnt(6)
	v_mfma_f32_16x16x32_bf16 v[64:67], v[232:235], v[12:15], v[64:67]
	v_cvt_pk_bf16_f32 v184, v80, v81
	v_mfma_f32_16x16x32_bf16 v[68:71], v[236:239], v[12:15], v[68:71]
	s_mov_b32 m0, s35
	s_add_i32 s51, s50, 0x10000
	v_cvt_pk_bf16_f32 v185, v82, v83
	v_mfma_f32_16x16x32_bf16 v[60:63], v[236:239], v[8:11], v[60:63]
	buffer_load_dwordx4 v125, s[36:39], s51 offen lds
	v_cvt_pk_bf16_f32 v186, v76, v77
	v_mfma_f32_16x16x32_bf16 v[56:59], v[232:235], v[8:11], v[56:59]
	v_cvt_pk_bf16_f32 v187, v78, v79
	ds_read_b128 v[232:235], v121 offset:51200
	ds_read_b128 v[236:239], v121 offset:52224
	s_waitcnt lgkmcnt(6)
	v_mfma_f32_16x16x32_bf16 v[64:67], v[240:243], v[16:19], v[64:67]
	v_cvt_pk_bf16_f32 v188, v84, v85
	v_mfma_f32_16x16x32_bf16 v[68:71], v[244:247], v[16:19], v[68:71]
	s_mov_b32 m0, s42
	s_add_i32 s51, s50, 0x12000
	v_cvt_pk_bf16_f32 v189, v86, v87
	v_mfma_f32_16x16x32_bf16 v[60:63], v[244:247], v[20:23], v[60:63]
	buffer_load_dwordx4 v125, s[36:39], s51 offen lds
	v_cvt_pk_bf16_f32 v190, v72, v73
	v_mfma_f32_16x16x32_bf16 v[56:59], v[240:243], v[20:23], v[56:59]
	v_cvt_pk_bf16_f32 v191, v74, v75
	ds_read_b128 v[240:243], v121 offset:53248
	ds_read_b128 v[244:247], v121 offset:54272
	s_waitcnt lgkmcnt(6)
	v_mfma_f32_16x16x32_bf16 v[64:67], v[248:251], v[24:27], v[64:67]
	v_pk_max_i16 v184, v184, 0
	v_mfma_f32_16x16x32_bf16 v[68:71], v[252:255], v[24:27], v[68:71]
	s_mov_b32 m0, s41
	s_add_i32 s51, s50, 0x14000
	v_pk_max_i16 v185, v185, 0
	v_mfma_f32_16x16x32_bf16 v[60:63], v[252:255], v[28:31], v[60:63]
	buffer_load_dwordx4 v125, s[36:39], s51 offen lds
	v_pk_max_i16 v186, v186, 0
	v_mfma_f32_16x16x32_bf16 v[56:59], v[248:251], v[28:31], v[56:59]
	v_pk_max_i16 v187, v187, 0
	ds_read_b128 v[248:251], v121 offset:55296
	ds_read_b128 v[252:255], v121 offset:56320
	s_waitcnt lgkmcnt(6)
	v_mfma_f32_16x16x32_bf16 v[64:67], v[224:227], v[32:35], v[64:67]
	v_pk_max_i16 v188, v188, 0
	v_mfma_f32_16x16x32_bf16 v[68:71], v[228:231], v[32:35], v[68:71]
	s_mov_b32 m0, s40
	s_add_i32 s51, s50, 0x16000
	v_pk_max_i16 v189, v189, 0
	v_mfma_f32_16x16x32_bf16 v[60:63], v[228:231], v[36:39], v[60:63]
	buffer_load_dwordx4 v125, s[36:39], s51 offen lds
	v_pk_max_i16 v190, v190, 0
	v_mfma_f32_16x16x32_bf16 v[56:59], v[224:227], v[36:39], v[56:59]
	v_pk_max_i16 v191, v191, 0
	ds_read_b128 v[224:227], v121 offset:57344
	ds_read_b128 v[228:231], v121 offset:58368
	s_waitcnt lgkmcnt(6)
	v_mfma_f32_16x16x32_bf16 v[64:67], v[232:235], v[40:43], v[64:67]
	ds_read_b128 v[80:83], v183 offset:640
	ds_read_b128 v[84:87], v183 offset:640
	ds_read_b128 v[76:79], v183 offset:704
	ds_read_b128 v[72:75], v183 offset:704
	v_mfma_f32_16x16x32_bf16 v[68:71], v[236:239], v[40:43], v[68:71]
	v_mfma_f32_16x16x32_bf16 v[60:63], v[236:239], v[44:47], v[60:63]
	v_mfma_f32_16x16x32_bf16 v[56:59], v[232:235], v[44:47], v[56:59]
	ds_read_b128 v[232:235], v121 offset:59392
	ds_read_b128 v[236:239], v121 offset:60416
	s_waitcnt lgkmcnt(10)
	v_mfma_f32_16x16x32_bf16 v[64:67], v[240:243], v[48:51], v[64:67]
	v_mfma_f32_16x16x32_bf16 v[68:71], v[244:247], v[48:51], v[68:71]
	v_mfma_f32_16x16x32_bf16 v[60:63], v[244:247], v[52:55], v[60:63]
	v_mfma_f32_16x16x32_bf16 v[56:59], v[240:243], v[52:55], v[56:59]
	ds_read_b128 v[240:243], v121 offset:61440
	ds_read_b128 v[244:247], v121 offset:62464
	s_waitcnt lgkmcnt(10)
	v_mfma_f32_16x16x32_bf16 v[64:67], v[248:251], v[112:115], v[64:67]
	v_mfma_f32_16x16x32_bf16 v[68:71], v[252:255], v[112:115], v[68:71]
	v_mfma_f32_16x16x32_bf16 v[60:63], v[252:255], v[116:119], v[60:63]
	v_mfma_f32_16x16x32_bf16 v[56:59], v[248:251], v[116:119], v[56:59]
	ds_read_b128 v[248:251], v121 offset:63488
	ds_read_b128 v[252:255], v121 offset:64512
	s_waitcnt lgkmcnt(6)
	v_mfma_f32_16x16x32_bf16 v[80:83], v[224:227], v[0:3], v[80:83]
	v_mfma_f32_16x16x32_bf16 v[76:79], v[228:231], v[0:3], v[76:79]
	v_mfma_f32_16x16x32_bf16 v[72:75], v[228:231], v[4:7], v[72:75]
	v_mfma_f32_16x16x32_bf16 v[84:87], v[224:227], v[4:7], v[84:87]
	ds_read_b128 v[224:227], v126 offset:57344
	ds_read_b128 v[228:231], v126 offset:58368
	s_waitcnt lgkmcnt(6)
	v_mfma_f32_16x16x32_bf16 v[80:83], v[232:235], v[12:15], v[80:83]
	v_cvt_pk_bf16_f32 v192, v64, v65
	v_mfma_f32_16x16x32_bf16 v[76:79], v[236:239], v[12:15], v[76:79]
	v_cvt_pk_bf16_f32 v193, v66, v67
	v_mfma_f32_16x16x32_bf16 v[72:75], v[236:239], v[8:11], v[72:75]
	v_cvt_pk_bf16_f32 v194, v68, v69
	v_mfma_f32_16x16x32_bf16 v[84:87], v[232:235], v[8:11], v[84:87]
	v_cvt_pk_bf16_f32 v195, v70, v71
	ds_read_b128 v[232:235], v126 offset:59392
	ds_read_b128 v[236:239], v126 offset:60416
	s_waitcnt lgkmcnt(6)
	v_mfma_f32_16x16x32_bf16 v[80:83], v[240:243], v[16:19], v[80:83]
	v_cvt_pk_bf16_f32 v196, v56, v57
	v_mfma_f32_16x16x32_bf16 v[76:79], v[244:247], v[16:19], v[76:79]
	v_cvt_pk_bf16_f32 v197, v58, v59
	v_mfma_f32_16x16x32_bf16 v[72:75], v[244:247], v[20:23], v[72:75]
	v_cvt_pk_bf16_f32 v198, v60, v61
	v_mfma_f32_16x16x32_bf16 v[84:87], v[240:243], v[20:23], v[84:87]
	v_cvt_pk_bf16_f32 v199, v62, v63
	ds_read_b128 v[240:243], v126 offset:61440
	ds_read_b128 v[244:247], v126 offset:62464
	s_waitcnt lgkmcnt(6)
	v_mfma_f32_16x16x32_bf16 v[80:83], v[248:251], v[24:27], v[80:83]
	v_pk_max_i16 v192, v192, 0
	v_mfma_f32_16x16x32_bf16 v[76:79], v[252:255], v[24:27], v[76:79]
	v_pk_max_i16 v193, v193, 0
	v_mfma_f32_16x16x32_bf16 v[72:75], v[252:255], v[28:31], v[72:75]
	v_pk_max_i16 v194, v194, 0
	v_mfma_f32_16x16x32_bf16 v[84:87], v[248:251], v[28:31], v[84:87]
	v_pk_max_i16 v195, v195, 0
	ds_read_b128 v[248:251], v126 offset:63488
	ds_read_b128 v[252:255], v126 offset:64512
	s_waitcnt lgkmcnt(6)
	v_mfma_f32_16x16x32_bf16 v[80:83], v[224:227], v[32:35], v[80:83]
	v_pk_max_i16 v196, v196, 0
	v_mfma_f32_16x16x32_bf16 v[76:79], v[228:231], v[32:35], v[76:79]
	v_pk_max_i16 v197, v197, 0
	v_mfma_f32_16x16x32_bf16 v[72:75], v[228:231], v[36:39], v[72:75]
	v_pk_max_i16 v198, v198, 0
	v_mfma_f32_16x16x32_bf16 v[84:87], v[224:227], v[36:39], v[84:87]
	v_pk_max_i16 v199, v199, 0
	s_waitcnt lgkmcnt(4)
	v_mfma_f32_16x16x32_bf16 v[80:83], v[232:235], v[40:43], v[80:83]
	ds_read_b128 v[64:67], v183 offset:768
	ds_read_b128 v[56:59], v183 offset:768
	ds_read_b128 v[68:71], v183 offset:832
	ds_read_b128 v[60:63], v183 offset:832
	v_mfma_f32_16x16x32_bf16 v[76:79], v[236:239], v[40:43], v[76:79]
	v_mfma_f32_16x16x32_bf16 v[72:75], v[236:239], v[44:47], v[72:75]
	v_mfma_f32_16x16x32_bf16 v[84:87], v[232:235], v[44:47], v[84:87]
.Lnerf_hid_b3:
	s_waitcnt vmcnt(0) lgkmcnt(0)
	s_barrier
	ds_read_b128 v[224:227], v121 offset:8192
	ds_read_b128 v[228:231], v121 offset:9216
	ds_read_b128 v[232:235], v121 offset:10240
	ds_read_b128 v[236:239], v121 offset:11264
	v_mfma_f32_16x16x32_bf16 v[80:83], v[240:243], v[48:51], v[80:83]
	v_mfma_f32_16x16x32_bf16 v[76:79], v[244:247], v[48:51], v[76:79]
	v_mfma_f32_16x16x32_bf16 v[72:75], v[244:247], v[52:55], v[72:75]
	v_mfma_f32_16x16x32_bf16 v[84:87], v[240:243], v[52:55], v[84:87]
	ds_read_b128 v[240:243], v121 offset:12288
	ds_read_b128 v[244:247], v121 offset:13312
	v_mfma_f32_16x16x32_bf16 v[80:83], v[248:251], v[112:115], v[80:83]
	v_mfma_f32_16x16x32_bf16 v[76:79], v[252:255], v[112:115], v[76:79]
	v_mfma_f32_16x16x32_bf16 v[72:75], v[252:255], v[116:119], v[72:75]
	v_mfma_f32_16x16x32_bf16 v[84:87], v[248:251], v[116:119], v[84:87]
	ds_read_b128 v[248:251], v121 offset:14336
	ds_read_b128 v[252:255], v121 offset:15360
	s_waitcnt lgkmcnt(6)
	v_mfma_f32_16x16x32_bf16 v[64:67], v[224:227], v[0:3], v[64:67]
	v_mfma_f32_16x16x32_bf16 v[68:71], v[228:231], v[0:3], v[68:71]
	v_mfma_f32_16x16x32_bf16 v[60:63], v[228:231], v[4:7], v[60:63]
	v_mfma_f32_16x16x32_bf16 v[56:59], v[224:227], v[4:7], v[56:59]
	ds_read_b128 v[224:227], v121 offset:16384
	ds_read_b128 v[228:231], v121 offset:17408
	s_waitcnt lgkmcnt(6)
	v_mfma_f32_16x16x32_bf16 v[64:67], v[232:235], v[12:15], v[64:67]
	v_cvt_pk_bf16_f32 v200, v80, v81
	v_mfma_f32_16x16x32_bf16 v[68:71], v[236:239], v[12:15], v[68:71]
	s_mov_b32 m0, s28
	s_add_i32 s51, s50, 0x18000
	v_cvt_pk_bf16_f32 v201, v82, v83
	v_mfma_f32_16x16x32_bf16 v[60:63], v[236:239], v[8:11], v[60:63]
	buffer_load_dwordx4 v125, s[36:39], s51 offen lds
	v_cvt_pk_bf16_f32 v202, v76, v77
	v_mfma_f32_16x16x32_bf16 v[56:59], v[232:235], v[8:11], v[56:59]
	v_cvt_pk_bf16_f32 v203, v78, v79
	ds_read_b128 v[232:235], v121 offset:18432
	ds_read_b128 v[236:239], v121 offset:19456
	s_waitcnt lgkmcnt(6)
	v_mfma_f32_16x16x32_bf16 v[64:67], v[240:243], v[16:19], v[64:67]
	v_cvt_pk_bf16_f32 v204, v84, v85
	v_mfma_f32_16x16x32_bf16 v[68:71], v[244:247], v[16:19], v[68:71]
	s_mov_b32 m0, s29
	s_add_i32 s51, s50, 0x1a000
	v_cvt_pk_bf16_f32 v205, v86, v87
	v_mfma_f32_16x16x32_bf16 v[60:63], v[244:247], v[20:23], v[60:63]
	buffer_load_dwordx4 v125, s[36:39], s51 offen lds
	v_cvt_pk_bf16_f32 v206, v72, v73
	v_mfma_f32_16x16x32_bf16 v[56:59], v[240:243], v[20:23], v[56:59]
	v_cvt_pk_bf16_f32 v207, v74, v75
	ds_read_b128 v[240:243], v121 offset:20480
	ds_read_b128 v[244:247], v121 offset:21504
	s_waitcnt lgkmcnt(6)
	v_mfma_f32_16x16x32_bf16 v[64:67], v[248:251], v[24:27], v[64:67]
	v_pk_max_i16 v200, v200, 0
	v_mfma_f32_16x16x32_bf16 v[68:71], v[252:255], v[24:27], v[68:71]
	s_mov_b32 m0, s33
	s_add_i32 s51, s50, 0x1c000
	v_pk_max_i16 v201, v201, 0
	v_mfma_f32_16x16x32_bf16 v[60:63], v[252:255], v[28:31], v[60:63]
	buffer_load_dwordx4 v125, s[36:39], s51 offen lds
	v_pk_max_i16 v202, v202, 0
	v_mfma_f32_16x16x32_bf16 v[56:59], v[248:251], v[28:31], v[56:59]
	v_pk_max_i16 v203, v203, 0
	ds_read_b128 v[248:251], v121 offset:22528
	ds_read_b128 v[252:255], v121 offset:23552
	s_waitcnt lgkmcnt(6)
	v_mfma_f32_16x16x32_bf16 v[64:67], v[224:227], v[32:35], v[64:67]
	v_pk_max_i16 v204, v204, 0
	v_mfma_f32_16x16x32_bf16 v[68:71], v[228:231], v[32:35], v[68:71]
	s_mov_b32 m0, s34
	s_add_i32 s51, s50, 0x1e000
	v_pk_max_i16 v205, v205, 0
	v_mfma_f32_16x16x32_bf16 v[60:63], v[228:231], v[36:39], v[60:63]
	buffer_load_dwordx4 v125, s[36:39], s51 offen lds
	v_pk_max_i16 v206, v206, 0
	v_mfma_f32_16x16x32_bf16 v[56:59], v[224:227], v[36:39], v[56:59]
	v_pk_max_i16 v207, v207, 0
	ds_read_b128 v[224:227], v121 offset:24576
	ds_read_b128 v[228:231], v121 offset:25600
	s_waitcnt lgkmcnt(6)
	v_mfma_f32_16x16x32_bf16 v[64:67], v[232:235], v[40:43], v[64:67]
	ds_read_b128 v[80:83], v183 offset:896
	ds_read_b128 v[84:87], v183 offset:896
	ds_read_b128 v[76:79], v183 offset:960
	ds_read_b128 v[72:75], v183 offset:960
	v_mfma_f32_16x16x32_bf16 v[68:71], v[236:239], v[40:43], v[68:71]
	v_mfma_f32_16x16x32_bf16 v[60:63], v[236:239], v[44:47], v[60:63]
	v_mfma_f32_16x16x32_bf16 v[56:59], v[232:235], v[44:47], v[56:59]
	ds_read_b128 v[232:235], v121 offset:26624
	ds_read_b128 v[236:239], v121 offset:27648
	s_waitcnt lgkmcnt(10)
	v_mfma_f32_16x16x32_bf16 v[64:67], v[240:243], v[48:51], v[64:67]
	v_mfma_f32_16x16x32_bf16 v[68:71], v[244:247], v[48:51], v[68:71]
	v_mfma_f32_16x16x32_bf16 v[60:63], v[244:247], v[52:55], v[60:63]
	v_mfma_f32_16x16x32_bf16 v[56:59], v[240:243], v[52:55], v[56:59]
	ds_read_b128 v[240:243], v121 offset:28672
	ds_read_b128 v[244:247], v121 offset:29696
	s_waitcnt lgkmcnt(10)
	v_mfma_f32_16x16x32_bf16 v[64:67], v[248:251], v[112:115], v[64:67]
	v_mfma_f32_16x16x32_bf16 v[68:71], v[252:255], v[112:115], v[68:71]
	v_mfma_f32_16x16x32_bf16 v[60:63], v[252:255], v[116:119], v[60:63]
	v_mfma_f32_16x16x32_bf16 v[56:59], v[248:251], v[116:119], v[56:59]
	ds_read_b128 v[248:251], v121 offset:30720
	ds_read_b128 v[252:255], v121 offset:31744
	s_waitcnt lgkmcnt(6)
	v_mfma_f32_16x16x32_bf16 v[80:83], v[224:227], v[0:3], v[80:83]
	v_mfma_f32_16x16x32_bf16 v[76:79], v[228:231], v[0:3], v[76:79]
	v_mfma_f32_16x16x32_bf16 v[72:75], v[228:231], v[4:7], v[72:75]
	v_mfma_f32_16x16x32_bf16 v[84:87], v[224:227], v[4:7], v[84:87]
	ds_read_b128 v[224:227], v121 offset:32768
	ds_read_b128 v[228:231], v121 offset:33792
	s_waitcnt lgkmcnt(6)
	v_mfma_f32_16x16x32_bf16 v[80:83], v[232:235], v[12:15], v[80:83]
	v_cvt_pk_bf16_f32 v208, v64, v65
	v_mfma_f32_16x16x32_bf16 v[76:79], v[236:239], v[12:15], v[76:79]
	v_cvt_pk_bf16_f32 v209, v66, v67
	v_mfma_f32_16x16x32_bf16 v[72:75], v[236:239], v[8:11], v[72:75]
	v_cvt_pk_bf16_f32 v210, v68, v69
	v_mfma_f32_16x16x32_bf16 v[84:87], v[232:235], v[8:11], v[84:87]
	v_cvt_pk_bf16_f32 v211, v70, v71
	ds_read_b128 v[232:235], v121 offset:34816
	ds_read_b128 v[236:239], v121 offset:35840
	s_waitcnt lgkmcnt(6)
	v_mfma_f32_16x16x32_bf16 v[80:83], v[240:243], v[16:19], v[80:83]
	v_cvt_pk_bf16_f32 v212, v56, v57
	v_mfma_f32_16x16x32_bf16 v[76:79], v[244:247], v[16:19], v[76:79]
	v_cvt_pk_bf16_f32 v213, v58, v59
	v_mfma_f32_16x16x32_bf16 v[72:75], v[244:247], v[20:23], v[72:75]
	v_cvt_pk_bf16_f32 v214, v60, v61
	v_mfma_f32_16x16x32_bf16 v[84:87], v[240:243], v[20:23], v[84:87]
	v_cvt_pk_bf16_f32 v215, v62, v63
	ds_read_b128 v[240:243], v121 offset:36864
	ds_read_b128 v[244:247], v121 offset:37888
	s_waitcnt lgkmcnt(6)
	v_mfma_f32_16x16x32_bf16 v[80:83], v[248:251], v[24:27], v[80:83]
	v_pk_max_i16 v208, v208, 0
	v_mfma_f32_16x16x32_bf16 v[76:79], v[252:255], v[24:27], v[76:79]
	v_pk_max_i16 v209, v209, 0
	v_mfma_f32_16x16x32_bf16 v[72:75], v[252:255], v[28:31], v[72:75]
	v_pk_max_i16 v210, v210, 0
	v_mfma_f32_16x16x32_bf16 v[84:87], v[248:251], v[28:31], v[84:87]
	v_pk_max_i16 v211, v211, 0
	ds_read_b128 v[248:251], v121 offset:38912
	ds_read_b128 v[252:255], v121 offset:39936
	s_waitcnt lgkmcnt(6)
	v_mfma_f32_16x16x32_bf16 v[80:83], v[224:227], v[32:35], v[80:83]
	v_pk_max_i16 v212, v212, 0
	v_mfma_f32_16x16x32_bf16 v[76:79], v[228:231], v[32:35], v[76:79]
	v_pk_max_i16 v213, v213, 0
	v_mfma_f32_16x16x32_bf16 v[72:75], v[228:231], v[36:39], v[72:75]
	v_pk_max_i16 v214, v214, 0
	v_mfma_f32_16x16x32_bf16 v[84:87], v[224:227], v[36:39], v[84:87]
	v_pk_max_i16 v215, v215, 0
	s_waitcnt lgkmcnt(4)
	v_mfma_f32_16x16x32_bf16 v[80:83], v[232:235], v[40:43], v[80:83]
	ds_read_b128 v[64:67], v183 offset:1024
	ds_read_b128 v[56:59], v183 offset:1024
	ds_read_b128 v[68:71], v183 offset:1088
	ds_read_b128 v[60:63], v183 offset:1088
	v_mfma_f32_16x16x32_bf16 v[76:79], v[236:239], v[40:43], v[76:79]
	v_mfma_f32_16x16x32_bf16 v[72:75], v[236:239], v[44:47], v[72:75]
	v_mfma_f32_16x16x32_bf16 v[84:87], v[232:235], v[44:47], v[84:87]
.Lnerf_hid_b4:
	s_waitcnt vmcnt(0) lgkmcnt(0)
	s_barrier
	ds_read_b128 v[224:227], v121 offset:40960
	ds_read_b128 v[228:231], v121 offset:41984
	ds_read_b128 v[232:235], v121 offset:43008
	ds_read_b128 v[236:239], v121 offset:44032
	v_mfma_f32_16x16x32_bf16 v[80:83], v[240:243], v[48:51], v[80:83]
	v_mfma_f32_16x16x32_bf16 v[76:79], v[244:247], v[48:51], v[76:79]
	v_mfma_f32_16x16x32_bf16 v[72:75], v[244:247], v[52:55], v[72:75]
	v_mfma_f32_16x16x32_bf16 v[84:87], v[240:243], v[52:55], v[84:87]
	ds_read_b128 v[240:243], v121 offset:45056
	ds_read_b128 v[244:247], v121 offset:46080
	v_mfma_f32_16x16x32_bf16 v[80:83], v[248:251], v[112:115], v[80:83]
	v_mfma_f32_16x16x32_bf16 v[76:79], v[252:255], v[112:115], v[76:79]
	v_mfma_f32_16x16x32_bf16 v[72:75], v[252:255], v[116:119], v[72:75]
	v_mfma_f32_16x16x32_bf16 v[84:87], v[248:251], v[116:119], v[84:87]
	ds_read_b128 v[248:251], v121 offset:47104
	ds_read_b128 v[252:255], v121 offset:48128
	s_waitcnt lgkmcnt(6)
	v_mfma_f32_16x16x32_bf16 v[64:67], v[224:227], v[88:91], v[64:67]
	v_mfma_f32_16x16x32_bf16 v[68:71], v[228:231], v[88:91], v[68:71]
	v_mfma_f32_16x16x32_bf16 v[60:63], v[228:231], v[92:95], v[60:63]
	v_mfma_f32_16x16x32_bf16 v[56:59], v[224:227], v[92:95], v[56:59]
	ds_read_b128 v[224:227], v121 offset:49152
	ds_read_b128 v[228:231], v121 offset:50176
	s_waitcnt lgkmcnt(6)
	v_mfma_f32_16x16x32_bf16 v[64:67], v[232:235], v[96:99], v[64:67]
	v_cvt_pk_bf16_f32 v216, v80, v81
	v_mfma_f32_16x16x32_bf16 v[68:71], v[236:239], v[96:99], v[68:71]
	s_mov_b32 m0, s35
	s_add_i32 s51, s50, 0x20000
	v_cvt_pk_bf16_f32 v217, v82, v83
	v_mfma_f32_16x16x32_bf16 v[60:63], v[236:239], v[100:103], v[60:63]
	buffer_load_dwordx4 v125, s[36:39], s51 offen lds
	v_cvt_pk_bf16_f32 v218, v76, v77
	v_mfma_f32_16x16x32_bf16 v[56:59], v[232:235], v[100:103], v[56:59]
	v_cvt_pk_bf16_f32 v219, v78, v79
	ds_read_b128 v[232:235], v121 offset:51200
	ds_read_b128 v[236:239], v121 offset:52224
	s_waitcnt lgkmcnt(6)
	v_mfma_f32_16x16x32_bf16 v[64:67], v[240:243], v[104:107], v[64:67]
	v_cvt_pk_bf16_f32 v220, v84, v85
	v_mfma_f32_16x16x32_bf16 v[68:71], v[244:247], v[104:107], v[68:71]
	s_mov_b32 m0, s42
	s_add_i32 s51, s50, 0x22000
	v_cvt_pk_bf16_f32 v221, v86, v87
	v_mfma_f32_16x16x32_bf16 v[60:63], v[244:247], v[108:111], v[60:63]
	buffer_load_dwordx4 v125, s[36:39], s51 offen lds
	v_cvt_pk_bf16_f32 v222, v72, v73
	v_mfma_f32_16x16x32_bf16 v[56:59], v[240:243], v[108:111], v[56:59]
	v_cvt_pk_bf16_f32 v223, v74, v75
	ds_read_b128 v[240:243], v121 offset:53248
	ds_read_b128 v[244:247], v121 offset:54272
	s_waitcnt lgkmcnt(6)
	v_mfma_f32_16x16x32_bf16 v[64:67], v[248:251], v[184:187], v[64:67]
	v_pk_max_i16 v216, v216, 0
	v_mfma_f32_16x16x32_bf16 v[68:71], v[252:255], v[184:187], v[68:71]
	s_mov_b32 m0, s41
	s_add_i32 s51, s50, 0x24000
	v_pk_max_i16 v217, v217, 0
	v_mfma_f32_16x16x32_bf16 v[60:63], v[252:255], v[188:191], v[60:63]
	buffer_load_dwordx4 v125, s[36:39], s51 offen lds
	v_pk_max_i16 v218, v218, 0
	v_mfma_f32_16x16x32_bf16 v[56:59], v[248:251], v[188:191], v[56:59]
	v_pk_max_i16 v219, v219, 0
	ds_read_b128 v[248:251], v121 offset:55296
	ds_read_b128 v[252:255], v121 offset:56320
	s_waitcnt lgkmcnt(6)
	v_mfma_f32_16x16x32_bf16 v[64:67], v[224:227], v[192:195], v[64:67]
	v_pk_max_i16 v220, v220, 0
	v_mfma_f32_16x16x32_bf16 v[68:71], v[228:231], v[192:195], v[68:71]
	s_mov_b32 m0, s40
	s_add_i32 s51, s50, 0x26000
	v_pk_max_i16 v221, v221, 0
	v_mfma_f32_16x16x32_bf16 v[60:63], v[228:231], v[196:199], v[60:63]
	buffer_load_dwordx4 v125, s[36:39], s51 offen lds
	v_pk_max_i16 v222, v222, 0
	v_mfma_f32_16x16x32_bf16 v[56:59], v[224:227], v[196:199], v[56:59]
	v_pk_max_i16 v223, v223, 0
	ds_read_b128 v[224:227], v121 offset:57344
	ds_read_b128 v[228:231], v121 offset:58368
	s_waitcnt lgkmcnt(6)
	v_mfma_f32_16x16x32_bf16 v[64:67], v[232:235], v[200:203], v[64:67]
	ds_read_b128 v[80:83], v183 offset:1152
	ds_read_b128 v[84:87], v183 offset:1152
	ds_read_b128 v[76:79], v183 offset:1216
	ds_read_b128 v[72:75], v183 offset:1216
	v_mfma_f32_16x16x32_bf16 v[68:71], v[236:239], v[200:203], v[68:71]
	v_mfma_f32_16x16x32_bf16 v[60:63], v[236:239], v[204:207], v[60:63]
	v_mfma_f32_16x16x32_bf16 v[56:59], v[232:235], v[204:207], v[56:59]
	ds_read_b128 v[232:235], v121 offset:59392
	ds_read_b128 v[236:239], v121 offset:60416
	s_waitcnt lgkmcnt(10)
	v_mfma_f32_16x16x32_bf16 v[64:67], v[240:243], v[208:211], v[64:67]
	v_mfma_f32_16x16x32_bf16 v[68:71], v[244:247], v[208:211], v[68:71]
	v_mfma_f32_16x16x32_bf16 v[60:63], v[244:247], v[212:215], v[60:63]
	v_mfma_f32_16x16x32_bf16 v[56:59], v[240:243], v[212:215], v[56:59]
	ds_read_b128 v[240:243], v121 offset:61440
	ds_read_b128 v[244:247], v121 offset:62464
	s_waitcnt lgkmcnt(10)
	v_mfma_f32_16x16x32_bf16 v[64:67], v[248:251], v[216:219], v[64:67]
	v_mfma_f32_16x16x32_bf16 v[68:71], v[252:255], v[216:219], v[68:71]
	v_mfma_f32_16x16x32_bf16 v[60:63], v[252:255], v[220:223], v[60:63]
	v_mfma_f32_16x16x32_bf16 v[56:59], v[248:251], v[220:223], v[56:59]
	ds_read_b128 v[248:251], v121 offset:63488
	ds_read_b128 v[252:255], v121 offset:64512
	s_waitcnt lgkmcnt(6)
	v_mfma_f32_16x16x32_bf16 v[80:83], v[224:227], v[88:91], v[80:83]
	v_mfma_f32_16x16x32_bf16 v[76:79], v[228:231], v[88:91], v[76:79]
	v_mfma_f32_16x16x32_bf16 v[72:75], v[228:231], v[92:95], v[72:75]
	v_mfma_f32_16x16x32_bf16 v[84:87], v[224:227], v[92:95], v[84:87]
	ds_read_b128 v[224:227], v126 offset:57344
	ds_read_b128 v[228:231], v126 offset:58368
	s_waitcnt lgkmcnt(6)
	v_mfma_f32_16x16x32_bf16 v[80:83], v[232:235], v[96:99], v[80:83]
	v_cvt_pk_bf16_f32 v0, v64, v65
	v_mfma_f32_16x16x32_bf16 v[76:79], v[236:239], v[96:99], v[76:79]
	v_cvt_pk_bf16_f32 v1, v66, v67
	v_mfma_f32_16x16x32_bf16 v[72:75], v[236:239], v[100:103], v[72:75]
	v_cvt_pk_bf16_f32 v2, v68, v69
	v_mfma_f32_16x16x32_bf16 v[84:87], v[232:235], v[100:103], v[84:87]
	v_cvt_pk_bf16_f32 v3, v70, v71
	ds_read_b128 v[232:235], v126 offset:59392
	ds_read_b128 v[236:239], v126 offset:60416
	s_waitcnt lgkmcnt(6)
	v_mfma_f32_16x16x32_bf16 v[80:83], v[240:243], v[104:107], v[80:83]
	v_cvt_pk_bf16_f32 v4, v56, v57
	v_mfma_f32_16x16x32_bf16 v[76:79], v[244:247], v[104:107], v[76:79]
	v_cvt_pk_bf16_f32 v5, v58, v59
	v_mfma_f32_16x16x32_bf16 v[72:75], v[244:247], v[108:111], v[72:75]
	v_cvt_pk_bf16_f32 v6, v60, v61
	v_mfma_f32_16x16x32_bf16 v[84:87], v[240:243], v[108:111], v[84:87]
	v_cvt_pk_bf16_f32 v7, v62, v63
	ds_read_b128 v[240:243], v126 offset:61440
	ds_read_b128 v[244:247], v126 offset:62464
	s_waitcnt lgkmcnt(6)
	v_mfma_f32_16x16x32_bf16 v[80:83], v[248:251], v[184:187], v[80:83]
	v_pk_max_i16 v0, v0, 0
	v_mfma_f32_16x16x32_bf16 v[76:79], v[252:255], v[184:187], v[76:79]
	v_pk_max_i16 v1, v1, 0
	v_mfma_f32_16x16x32_bf16 v[72:75], v[252:255], v[188:191], v[72:75]
	v_pk_max_i16 v2, v2, 0
	v_mfma_f32_16x16x32_bf16 v[84:87], v[248:251], v[188:191], v[84:87]
	v_pk_max_i16 v3, v3, 0
	ds_read_b128 v[248:251], v126 offset:63488
	ds_read_b128 v[252:255], v126 offset:64512
	s_waitcnt lgkmcnt(6)
	v_mfma_f32_16x16x32_bf16 v[80:83], v[224:227], v[192:195], v[80:83]
	v_pk_max_i16 v4, v4, 0
	v_mfma_f32_16x16x32_bf16 v[76:79], v[228:231], v[192:195], v[76:79]
	v_pk_max_i16 v5, v5, 0
	v_mfma_f32_16x16x32_bf16 v[72:75], v[228:231], v[196:199], v[72:75]
	v_pk_max_i16 v6, v6, 0
	v_mfma_f32_16x16x32_bf16 v[84:87], v[224:227], v[196:199], v[84:87]
	v_pk_max_i16 v7, v7, 0
	s_waitcnt lgkmcnt(4)
	v_mfma_f32_16x16x32_bf16 v[80:83], v[232:235], v[200:203], v[80:83]
	ds_read_b128 v[64:67], v183 offset:1280
	ds_read_b128 v[56:59], v183 offset:1280
	ds_read_b128 v[68:71], v183 offset:1344
	ds_read_b128 v[60:63], v183 offset:1344
	v_mfma_f32_16x16x32_bf16 v[76:79], v[236:239], v[200:203], v[76:79]
	v_mfma_f32_16x16x32_bf16 v[72:75], v[236:239], v[204:207], v[72:75]
	v_mfma_f32_16x16x32_bf16 v[84:87], v[232:235], v[204:207], v[84:87]
.Lnerf_hid_b5:
	s_waitcnt vmcnt(0) lgkmcnt(0)
	s_barrier
	ds_read_b128 v[224:227], v121 offset:8192
	ds_read_b128 v[228:231], v121 offset:9216
	ds_read_b128 v[232:235], v121 offset:10240
	ds_read_b128 v[236:239], v121 offset:11264
	v_mfma_f32_16x16x32_bf16 v[80:83], v[240:243], v[208:211], v[80:83]
	v_mfma_f32_16x16x32_bf16 v[76:79], v[244:247], v[208:211], v[76:79]
	v_mfma_f32_16x16x32_bf16 v[72:75], v[244:247], v[212:215], v[72:75]
	v_mfma_f32_16x16x32_bf16 v[84:87], v[240:243], v[212:215], v[84:87]
	ds_read_b128 v[240:243], v121 offset:12288
	ds_read_b128 v[244:247], v121 offset:13312
	v_mfma_f32_16x16x32_bf16 v[80:83], v[248:251], v[216:219], v[80:83]
	v_mfma_f32_16x16x32_bf16 v[76:79], v[252:255], v[216:219], v[76:79]
	v_mfma_f32_16x16x32_bf16 v[72:75], v[252:255], v[220:223], v[72:75]
	v_mfma_f32_16x16x32_bf16 v[84:87], v[248:251], v[220:223], v[84:87]
	ds_read_b128 v[248:251], v121 offset:14336
	ds_read_b128 v[252:255], v121 offset:15360
	s_waitcnt lgkmcnt(6)
	v_mfma_f32_16x16x32_bf16 v[64:67], v[224:227], v[88:91], v[64:67]
	v_mfma_f32_16x16x32_bf16 v[68:71], v[228:231], v[88:91], v[68:71]
	v_mfma_f32_16x16x32_bf16 v[60:63], v[228:231], v[92:95], v[60:63]
	v_mfma_f32_16x16x32_bf16 v[56:59], v[224:227], v[92:95], v[56:59]
	ds_read_b128 v[224:227], v121 offset:16384
	ds_read_b128 v[228:231], v121 offset:17408
	s_waitcnt lgkmcnt(6)
	v_mfma_f32_16x16x32_bf16 v[64:67], v[232:235], v[96:99], v[64:67]
	v_cvt_pk_bf16_f32 v12, v80, v81
	v_mfma_f32_16x16x32_bf16 v[68:71], v[236:239], v[96:99], v[68:71]
	s_mov_b32 m0, s28
	s_add_i32 s51, s50, 0x28000
	v_cvt_pk_bf16_f32 v13, v82, v83
	v_mfma_f32_16x16x32_bf16 v[60:63], v[236:239], v[100:103], v[60:63]
	buffer_load_dwordx4 v125, s[36:39], s51 offen lds
	v_cvt_pk_bf16_f32 v14, v76, v77
	v_mfma_f32_16x16x32_bf16 v[56:59], v[232:235], v[100:103], v[56:59]
	v_cvt_pk_bf16_f32 v15, v78, v79
	ds_read_b128 v[232:235], v121 offset:18432
	ds_read_b128 v[236:239], v121 offset:19456
	s_waitcnt lgkmcnt(6)
	v_mfma_f32_16x16x32_bf16 v[64:67], v[240:243], v[104:107], v[64:67]
	v_cvt_pk_bf16_f32 v8, v84, v85
	v_mfma_f32_16x16x32_bf16 v[68:71], v[244:247], v[104:107], v[68:71]
	s_mov_b32 m0, s29
	s_add_i32 s51, s50, 0x2a000
	v_cvt_pk_bf16_f32 v9, v86, v87
	v_mfma_f32_16x16x32_bf16 v[60:63], v[244:247], v[108:111], v[60:63]
	buffer_load_dwordx4 v125, s[36:39], s51 offen lds
	v_cvt_pk_bf16_f32 v10, v72, v73
	v_mfma_f32_16x16x32_bf16 v[56:59], v[240:243], v[108:111], v[56:59]
	v_cvt_pk_bf16_f32 v11, v74, v75
	ds_read_b128 v[240:243], v121 offset:20480
	ds_read_b128 v[244:247], v121 offset:21504
	s_waitcnt lgkmcnt(6)
	v_mfma_f32_16x16x32_bf16 v[64:67], v[248:251], v[184:187], v[64:67]
	v_pk_max_i16 v12, v12, 0
	v_mfma_f32_16x16x32_bf16 v[68:71], v[252:255], v[184:187], v[68:71]
	s_mov_b32 m0, s33
	s_add_i32 s51, s50, 0x2c000
	v_pk_max_i16 v13, v13, 0
	v_mfma_f32_16x16x32_bf16 v[60:63], v[252:255], v[188:191], v[60:63]
	buffer_load_dwordx4 v125, s[36:39], s51 offen lds
	v_pk_max_i16 v14, v14, 0
	v_mfma_f32_16x16x32_bf16 v[56:59], v[248:251], v[188:191], v[56:59]
	v_pk_max_i16 v15, v15, 0
	ds_read_b128 v[248:251], v121 offset:22528
	ds_read_b128 v[252:255], v121 offset:23552
	s_waitcnt lgkmcnt(6)
	v_mfma_f32_16x16x32_bf16 v[64:67], v[224:227], v[192:195], v[64:67]
	v_pk_max_i16 v8, v8, 0
	v_mfma_f32_16x16x32_bf16 v[68:71], v[228:231], v[192:195], v[68:71]
	s_mov_b32 m0, s34
	s_add_i32 s51, s50, 0x2e000
	v_pk_max_i16 v9, v9, 0
	v_mfma_f32_16x16x32_bf16 v[60:63], v[228:231], v[196:199], v[60:63]
	buffer_load_dwordx4 v125, s[36:39], s51 offen lds
	v_pk_max_i16 v10, v10, 0
	v_mfma_f32_16x16x32_bf16 v[56:59], v[224:227], v[196:199], v[56:59]
	v_pk_max_i16 v11, v11, 0
	ds_read_b128 v[224:227], v121 offset:24576
	ds_read_b128 v[228:231], v121 offset:25600
	s_waitcnt lgkmcnt(6)
	v_mfma_f32_16x16x32_bf16 v[64:67], v[232:235], v[200:203], v[64:67]
	ds_read_b128 v[80:83], v183 offset:1408
	ds_read_b128 v[84:87], v183 offset:1408
	ds_read_b128 v[76:79], v183 offset:1472
	ds_read_b128 v[72:75], v183 offset:1472
	v_mfma_f32_16x16x32_bf16 v[68:71], v[236:239], v[200:203], v[68:71]
	v_mfma_f32_16x16x32_bf16 v[60:63], v[236:239], v[204:207], v[60:63]
	v_mfma_f32_16x16x32_bf16 v[56:59], v[232:235], v[204:207], v[56:59]
	ds_read_b128 v[232:235], v121 offset:26624
	ds_read_b128 v[236:239], v121 offset:27648
	s_waitcnt lgkmcnt(10)
	v_mfma_f32_16x16x32_bf16 v[64:67], v[240:243], v[208:211], v[64:67]
	v_mfma_f32_16x16x32_bf16 v[68:71], v[244:247], v[208:211], v[68:71]
	v_mfma_f32_16x16x32_bf16 v[60:63], v[244:247], v[212:215], v[60:63]
	v_mfma_f32_16x16x32_bf16 v[56:59], v[240:243], v[212:215], v[56:59]
	ds_read_b128 v[240:243], v121 offset:28672
	ds_read_b128 v[244:247], v121 offset:29696
	s_waitcnt lgkmcnt(10)
	v_mfma_f32_16x16x32_bf16 v[64:67], v[248:251], v[216:219], v[64:67]
	v_mfma_f32_16x16x32_bf16 v[68:71], v[252:255], v[216:219], v[68:71]
	v_mfma_f32_16x16x32_bf16 v[60:63], v[252:255], v[220:223], v[60:63]
	v_mfma_f32_16x16x32_bf16 v[56:59], v[248:251], v[220:223], v[56:59]
	ds_read_b128 v[248:251], v121 offset:30720
	ds_read_b128 v[252:255], v121 offset:31744
	s_waitcnt lgkmcnt(6)
	v_mfma_f32_16x16x32_bf16 v[80:83], v[224:227], v[88:91], v[80:83]
	v_mfma_f32_16x16x32_bf16 v[76:79], v[228:231], v[88:91], v[76:79]
	v_mfma_f32_16x16x32_bf16 v[72:75], v[228:231], v[92:95], v[72:75]
	v_mfma_f32_16x16x32_bf16 v[84:87], v[224:227], v[92:95], v[84:87]
	ds_read_b128 v[224:227], v121 offset:32768
	ds_read_b128 v[228:231], v121 offset:33792
	s_waitcnt lgkmcnt(6)
	v_mfma_f32_16x16x32_bf16 v[80:83], v[232:235], v[96:99], v[80:83]
	v_cvt_pk_bf16_f32 v16, v64, v65
	v_mfma_f32_16x16x32_bf16 v[76:79], v[236:239], v[96:99], v[76:79]
	v_cvt_pk_bf16_f32 v17, v66, v67
	v_mfma_f32_16x16x32_bf16 v[72:75], v[236:239], v[100:103], v[72:75]
	v_cvt_pk_bf16_f32 v18, v68, v69
	v_mfma_f32_16x16x32_bf16 v[84:87], v[232:235], v[100:103], v[84:87]
	v_cvt_pk_bf16_f32 v19, v70, v71
	ds_read_b128 v[232:235], v121 offset:34816
	ds_read_b128 v[236:239], v121 offset:35840
	s_waitcnt lgkmcnt(6)
	v_mfma_f32_16x16x32_bf16 v[80:83], v[240:243], v[104:107], v[80:83]
	v_cvt_pk_bf16_f32 v20, v56, v57
	v_mfma_f32_16x16x32_bf16 v[76:79], v[244:247], v[104:107], v[76:79]
	v_cvt_pk_bf16_f32 v21, v58, v59
	v_mfma_f32_16x16x32_bf16 v[72:75], v[244:247], v[108:111], v[72:75]
	v_cvt_pk_bf16_f32 v22, v60, v61
	v_mfma_f32_16x16x32_bf16 v[84:87], v[240:243], v[108:111], v[84:87]
	v_cvt_pk_bf16_f32 v23, v62, v63
	ds_read_b128 v[240:243], v121 offset:36864
	ds_read_b128 v[244:247], v121 offset:37888
	s_waitcnt lgkmcnt(6)
	v_mfma_f32_16x16x32_bf16 v[80:83], v[248:251], v[184:187], v[80:83]
	v_pk_max_i16 v16, v16, 0
	v_mfma_f32_16x16x32_bf16 v[76:79], v[252:255], v[184:187], v[76:79]
	v_pk_max_i16 v17, v17, 0
	v_mfma_f32_16x16x32_bf16 v[72:75], v[252:255], v[188:191], v[72:75]
	v_pk_max_i16 v18, v18, 0
	v_mfma_f32_16x16x32_bf16 v[84:87], v[248:251], v[188:191], v[84:87]
	v_pk_max_i16 v19, v19, 0
	ds_read_b128 v[248:251], v121 offset:38912
	ds_read_b128 v[252:255], v121 offset:39936
	s_waitcnt lgkmcnt(6)
	v_mfma_f32_16x16x32_bf16 v[80:83], v[224:227], v[192:195], v[80:83]
	v_pk_max_i16 v20, v20, 0
	v_mfma_f32_16x16x32_bf16 v[76:79], v[228:231], v[192:195], v[76:79]
	v_pk_max_i16 v21, v21, 0
	v_mfma_f32_16x16x32_bf16 v[72:75], v[228:231], v[196:199], v[72:75]
	v_pk_max_i16 v22, v22, 0
	v_mfma_f32_16x16x32_bf16 v[84:87], v[224:227], v[196:199], v[84:87]
	v_pk_max_i16 v23, v23, 0
	s_waitcnt lgkmcnt(4)
	v_mfma_f32_16x16x32_bf16 v[80:83], v[232:235], v[200:203], v[80:83]
	ds_read_b128 v[64:67], v183 offset:1536
	ds_read_b128 v[56:59], v183 offset:1536
	ds_read_b128 v[68:71], v183 offset:1600
	ds_read_b128 v[60:63], v183 offset:1600
	v_mfma_f32_16x16x32_bf16 v[76:79], v[236:239], v[200:203], v[76:79]
	v_mfma_f32_16x16x32_bf16 v[72:75], v[236:239], v[204:207], v[72:75]
	v_mfma_f32_16x16x32_bf16 v[84:87], v[232:235], v[204:207], v[84:87]
.Lnerf_hid_b6:
	s_waitcnt vmcnt(0) lgkmcnt(0)
	s_barrier
	ds_read_b128 v[224:227], v121 offset:40960
	ds_read_b128 v[228:231], v121 offset:41984
	ds_read_b128 v[232:235], v121 offset:43008
	ds_read_b128 v[236:239], v121 offset:44032
	v_mfma_f32_16x16x32_bf16 v[80:83], v[240:243], v[208:211], v[80:83]
	v_mfma_f32_16x16x32_bf16 v[76:79], v[244:247], v[208:211], v[76:79]
	v_mfma_f32_16x16x32_bf16 v[72:75], v[244:247], v[212:215], v[72:75]
	v_mfma_f32_16x16x32_bf16 v[84:87], v[240:243], v[212:215], v[84:87]
	ds_read_b128 v[240:243], v121 offset:45056
	ds_read_b128 v[244:247], v121 offset:46080
	v_mfma_f32_16x16x32_bf16 v[80:83], v[248:251], v[216:219], v[80:83]
	v_mfma_f32_16x16x32_bf16 v[76:79], v[252:255], v[216:219], v[76:79]
	v_mfma_f32_16x16x32_bf16 v[72:75], v[252:255], v[220:223], v[72:75]
	v_mfma_f32_16x16x32_bf16 v[84:87], v[248:251], v[220:223], v[84:87]
	ds_read_b128 v[248:251], v121 offset:47104
	ds_read_b128 v[252:255], v121 offset:48128
	s_waitcnt lgkmcnt(6)
	v_mfma_f32_16x16x32_bf16 v[64:67], v[224:227], v[88:91], v[64:67]
	v_mfma_f32_16x16x32_bf16 v[68:71], v[228:231], v[88:91], v[68:71]
	v_mfma_f32_16x16x32_bf16 v[60:63], v[228:231], v[92:95], v[60:63]
	v_mfma_f32_16x16x32_bf16 v[56:59], v[224:227], v[92:95], v[56:59]
	ds_read_b128 v[224:227], v121 offset:49152
	ds_read_b128 v[228:231], v121 offset:50176
	s_waitcnt lgkmcnt(6)
	v_mfma_f32_16x16x32_bf16 v[64:67], v[232:235], v[96:99], v[64:67]
	v_cvt_pk_bf16_f32 v24, v80, v81
	v_mfma_f32_16x16x32_bf16 v[68:71], v[236:239], v[96:99], v[68:71]
	s_mov_b32 m0, s35
	s_add_i32 s51, s50, 0x30000
	v_cvt_pk_bf16_f32 v25, v82, v83
	v_mfma_f32_16x16x32_bf16 v[60:63], v[236:239], v[100:103], v[60:63]
	buffer_load_dwordx4 v125, s[36:39], s51 offen lds
	v_cvt_pk_bf16_f32 v26, v76, v77
	v_mfma_f32_16x16x32_bf16 v[56:59], v[232:235], v[100:103], v[56:59]
	v_cvt_pk_bf16_f32 v27, v78, v79
	ds_read_b128 v[232:235], v121 offset:51200
	ds_read_b128 v[236:239], v121 offset:52224
	s_waitcnt lgkmcnt(6)
	v_mfma_f32_16x16x32_bf16 v[64:67], v[240:243], v[104:107], v[64:67]
	v_cvt_pk_bf16_f32 v28, v84, v85
	v_mfma_f32_16x16x32_bf16 v[68:71], v[244:247], v[104:107], v[68:71]
	s_mov_b32 m0, s42
	s_add_i32 s51, s50, 0x32000
	v_cvt_pk_bf16_f32 v29, v86, v87
	v_mfma_f32_16x16x32_bf16 v[60:63], v[244:247], v[108:111], v[60:63]
	buffer_load_dwordx4 v125, s[36:39], s51 offen lds
	v_cvt_pk_bf16_f32 v30, v72, v73
	v_mfma_f32_16x16x32_bf16 v[56:59], v[240:243], v[108:111], v[56:59]
	v_cvt_pk_bf16_f32 v31, v74, v75
	ds_read_b128 v[240:243], v121 offset:53248
	ds_read_b128 v[244:247], v121 offset:54272
	s_waitcnt lgkmcnt(6)
	v_mfma_f32_16x16x32_bf16 v[64:67], v[248:251], v[184:187], v[64:67]
	v_pk_max_i16 v24, v24, 0
	v_mfma_f32_16x16x32_bf16 v[68:71], v[252:255], v[184:187], v[68:71]
	s_mov_b32 m0, s41
	s_add_i32 s51, s50, 0x34000
	v_pk_max_i16 v25, v25, 0
	v_mfma_f32_16x16x32_bf16 v[60:63], v[252:255], v[188:191], v[60:63]
	buffer_load_dwordx4 v125, s[36:39], s51 offen lds
	v_pk_max_i16 v26, v26, 0
	v_mfma_f32_16x16x32_bf16 v[56:59], v[248:251], v[188:191], v[56:59]
	v_pk_max_i16 v27, v27, 0
	ds_read_b128 v[248:251], v121 offset:55296
	ds_read_b128 v[252:255], v121 offset:56320
	s_waitcnt lgkmcnt(6)
	v_mfma_f32_16x16x32_bf16 v[64:67], v[224:227], v[192:195], v[64:67]
	v_pk_max_i16 v28, v28, 0
	v_mfma_f32_16x16x32_bf16 v[68:71], v[228:231], v[192:195], v[68:71]
	s_mov_b32 m0, s40
	s_add_i32 s51, s50, 0x36000
	v_pk_max_i16 v29, v29, 0
	v_mfma_f32_16x16x32_bf16 v[60:63], v[228:231], v[196:199], v[60:63]
	buffer_load_dwordx4 v125, s[36:39], s51 offen lds
	v_pk_max_i16 v30, v30, 0
	v_mfma_f32_16x16x32_bf16 v[56:59], v[224:227], v[196:199], v[56:59]
	v_pk_max_i16 v31, v31, 0
	ds_read_b128 v[224:227], v121 offset:57344
	ds_read_b128 v[228:231], v121 offset:58368
	s_waitcnt lgkmcnt(6)
	v_mfma_f32_16x16x32_bf16 v[64:67], v[232:235], v[200:203], v[64:67]
	ds_read_b128 v[80:83], v183 offset:1664
	ds_read_b128 v[84:87], v183 offset:1664
	ds_read_b128 v[76:79], v183 offset:1728
	ds_read_b128 v[72:75], v183 offset:1728
	v_mfma_f32_16x16x32_bf16 v[68:71], v[236:239], v[200:203], v[68:71]
	v_mfma_f32_16x16x32_bf16 v[60:63], v[236:239], v[204:207], v[60:63]
	v_mfma_f32_16x16x32_bf16 v[56:59], v[232:235], v[204:207], v[56:59]
	ds_read_b128 v[232:235], v121 offset:59392
	ds_read_b128 v[236:239], v121 offset:60416
	s_waitcnt lgkmcnt(10)
	v_mfma_f32_16x16x32_bf16 v[64:67], v[240:243], v[208:211], v[64:67]
	v_mfma_f32_16x16x32_bf16 v[68:71], v[244:247], v[208:211], v[68:71]
	v_mfma_f32_16x16x32_bf16 v[60:63], v[244:247], v[212:215], v[60:63]
	v_mfma_f32_16x16x32_bf16 v[56:59], v[240:243], v[212:215], v[56:59]
	ds_read_b128 v[240:243], v121 offset:61440
	ds_read_b128 v[244:247], v121 offset:62464
	s_waitcnt lgkmcnt(10)
	v_mfma_f32_16x16x32_bf16 v[64:67], v[248:251], v[216:219], v[64:67]
	v_mfma_f32_16x16x32_bf16 v[68:71], v[252:255], v[216:219], v[68:71]
	v_mfma_f32_16x16x32_bf16 v[60:63], v[252:255], v[220:223], v[60:63]
	v_mfma_f32_16x16x32_bf16 v[56:59], v[248:251], v[220:223], v[56:59]
	ds_read_b128 v[248:251], v121 offset:63488
	ds_read_b128 v[252:255], v121 offset:64512
	s_waitcnt lgkmcnt(6)
	v_mfma_f32_16x16x32_bf16 v[80:83], v[224:227], v[88:91], v[80:83]
	v_mfma_f32_16x16x32_bf16 v[76:79], v[228:231], v[88:91], v[76:79]
	v_mfma_f32_16x16x32_bf16 v[72:75], v[228:231], v[92:95], v[72:75]
	v_mfma_f32_16x16x32_bf16 v[84:87], v[224:227], v[92:95], v[84:87]
	ds_read_b128 v[224:227], v126 offset:57344
	ds_read_b128 v[228:231], v126 offset:58368
	s_waitcnt lgkmcnt(6)
	v_mfma_f32_16x16x32_bf16 v[80:83], v[232:235], v[96:99], v[80:83]
	v_cvt_pk_bf16_f32 v32, v64, v65
	v_mfma_f32_16x16x32_bf16 v[76:79], v[236:239], v[96:99], v[76:79]
	v_cvt_pk_bf16_f32 v33, v66, v67
	v_mfma_f32_16x16x32_bf16 v[72:75], v[236:239], v[100:103], v[72:75]
	v_cvt_pk_bf16_f32 v34, v68, v69
	v_mfma_f32_16x16x32_bf16 v[84:87], v[232:235], v[100:103], v[84:87]
	v_cvt_pk_bf16_f32 v35, v70, v71
	ds_read_b128 v[232:235], v126 offset:59392
	ds_read_b128 v[236:239], v126 offset:60416
	s_waitcnt lgkmcnt(6)
	v_mfma_f32_16x16x32_bf16 v[80:83], v[240:243], v[104:107], v[80:83]
	v_cvt_pk_bf16_f32 v36, v56, v57
	v_mfma_f32_16x16x32_bf16 v[76:79], v[244:247], v[104:107], v[76:79]
	v_cvt_pk_bf16_f32 v37, v58, v59
	v_mfma_f32_16x16x32_bf16 v[72:75], v[244:247], v[108:111], v[72:75]
	v_cvt_pk_bf16_f32 v38, v60, v61
	v_mfma_f32_16x16x32_bf16 v[84:87], v[240:243], v[108:111], v[84:87]
	v_cvt_pk_bf16_f32 v39, v62, v63
	ds_read_b128 v[240:243], v126 offset:61440
	ds_read_b128 v[244:247], v126 offset:62464
	s_waitcnt lgkmcnt(6)
	v_mfma_f32_16x16x32_bf16 v[80:83], v[248:251], v[184:187], v[80:83]
	v_pk_max_i16 v32, v32, 0
	v_mfma_f32_16x16x32_bf16 v[76:79], v[252:255], v[184:187], v[76:79]
	v_pk_max_i16 v33, v33, 0
	v_mfma_f32_16x16x32_bf16 v[72:75], v[252:255], v[188:191], v[72:75]
	v_pk_max_i16 v34, v34, 0
	v_mfma_f32_16x16x32_bf16 v[84:87], v[248:251], v[188:191], v[84:87]
	v_pk_max_i16 v35, v35, 0
	ds_read_b128 v[248:251], v126 offset:63488
	ds_read_b128 v[252:255], v126 offset:64512
	s_waitcnt lgkmcnt(6)
	v_mfma_f32_16x16x32_bf16 v[80:83], v[224:227], v[192:195], v[80:83]
	v_pk_max_i16 v36, v36, 0
	v_mfma_f32_16x16x32_bf16 v[76:79], v[228:231], v[192:195], v[76:79]
	v_pk_max_i16 v37, v37, 0
	v_mfma_f32_16x16x32_bf16 v[72:75], v[228:231], v[196:199], v[72:75]
	v_pk_max_i16 v38, v38, 0
	v_mfma_f32_16x16x32_bf16 v[84:87], v[224:227], v[196:199], v[84:87]
	v_pk_max_i16 v39, v39, 0
	s_waitcnt lgkmcnt(4)
	v_mfma_f32_16x16x32_bf16 v[80:83], v[232:235], v[200:203], v[80:83]
	ds_read_b128 v[64:67], v183 offset:1792
	ds_read_b128 v[56:59], v183 offset:1792
	ds_read_b128 v[68:71], v183 offset:1856
	ds_read_b128 v[60:63], v183 offset:1856
	v_mfma_f32_16x16x32_bf16 v[76:79], v[236:239], v[200:203], v[76:79]
	v_mfma_f32_16x16x32_bf16 v[72:75], v[236:239], v[204:207], v[72:75]
	v_mfma_f32_16x16x32_bf16 v[84:87], v[232:235], v[204:207], v[84:87]
.Lnerf_hid_b7:
	s_waitcnt vmcnt(0) lgkmcnt(0)
	s_barrier
	ds_read_b128 v[224:227], v121 offset:8192
	ds_read_b128 v[228:231], v121 offset:9216
	ds_read_b128 v[232:235], v121 offset:10240
	ds_read_b128 v[236:239], v121 offset:11264
	v_mfma_f32_16x16x32_bf16 v[80:83], v[240:243], v[208:211], v[80:83]
	v_mfma_f32_16x16x32_bf16 v[76:79], v[244:247], v[208:211], v[76:79]
	v_mfma_f32_16x16x32_bf16 v[72:75], v[244:247], v[212:215], v[72:75]
	v_mfma_f32_16x16x32_bf16 v[84:87], v[240:243], v[212:215], v[84:87]
	ds_read_b128 v[240:243], v121 offset:12288
	ds_read_b128 v[244:247], v121 offset:13312
	v_mfma_f32_16x16x32_bf16 v[80:83], v[248:251], v[216:219], v[80:83]
	v_mfma_f32_16x16x32_bf16 v[76:79], v[252:255], v[216:219], v[76:79]
	v_mfma_f32_16x16x32_bf16 v[72:75], v[252:255], v[220:223], v[72:75]
	v_mfma_f32_16x16x32_bf16 v[84:87], v[248:251], v[220:223], v[84:87]
	ds_read_b128 v[248:251], v121 offset:14336
	ds_read_b128 v[252:255], v121 offset:15360
	s_waitcnt lgkmcnt(6)
	v_mfma_f32_16x16x32_bf16 v[64:67], v[224:227], v[88:91], v[64:67]
	v_mfma_f32_16x16x32_bf16 v[68:71], v[228:231], v[88:91], v[68:71]
	v_mfma_f32_16x16x32_bf16 v[60:63], v[228:231], v[92:95], v[60:63]
	v_mfma_f32_16x16x32_bf16 v[56:59], v[224:227], v[92:95], v[56:59]
	ds_read_b128 v[224:227], v121 offset:16384
	ds_read_b128 v[228:231], v121 offset:17408
	s_waitcnt lgkmcnt(6)
	v_mfma_f32_16x16x32_bf16 v[64:67], v[232:235], v[96:99], v[64:67]
	v_cvt_pk_bf16_f32 v40, v80, v81
	v_mfma_f32_16x16x32_bf16 v[68:71], v[236:239], v[96:99], v[68:71]
	s_mov_b32 m0, s28
	s_add_i32 s51, s50, 0x38000
	v_cvt_pk_bf16_f32 v41, v82, v83
	v_mfma_f32_16x16x32_bf16 v[60:63], v[236:239], v[100:103], v[60:63]
	buffer_load_dwordx4 v125, s[36:39], s51 offen lds
	v_cvt_pk_bf16_f32 v42, v76, v77
	v_mfma_f32_16x16x32_bf16 v[56:59], v[232:235], v[100:103], v[56:59]
	v_cvt_pk_bf16_f32 v43, v78, v79
	ds_read_b128 v[232:235], v121 offset:18432
	ds_read_b128 v[236:239], v121 offset:19456
	s_waitcnt lgkmcnt(6)
	v_mfma_f32_16x16x32_bf16 v[64:67], v[240:243], v[104:107], v[64:67]
	v_cvt_pk_bf16_f32 v44, v84, v85
	v_mfma_f32_16x16x32_bf16 v[68:71], v[244:247], v[104:107], v[68:71]
	s_mov_b32 m0, s29
	s_add_i32 s51, s50, 0x3a000
	v_cvt_pk_bf16_f32 v45, v86, v87
	v_mfma_f32_16x16x32_bf16 v[60:63], v[244:247], v[108:111], v[60:63]
	buffer_load_dwordx4 v125, s[36:39], s51 offen lds
	v_cvt_pk_bf16_f32 v46, v72, v73
	v_mfma_f32_16x16x32_bf16 v[56:59], v[240:243], v[108:111], v[56:59]
	v_cvt_pk_bf16_f32 v47, v74, v75
	ds_read_b128 v[240:243], v121 offset:20480
	ds_read_b128 v[244:247], v121 offset:21504
	s_waitcnt lgkmcnt(6)
	v_mfma_f32_16x16x32_bf16 v[64:67], v[248:251], v[184:187], v[64:67]
	v_pk_max_i16 v40, v40, 0
	v_mfma_f32_16x16x32_bf16 v[68:71], v[252:255], v[184:187], v[68:71]
	s_mov_b32 m0, s33
	s_add_i32 s51, s50, 0x3c000
	v_pk_max_i16 v41, v41, 0
	v_mfma_f32_16x16x32_bf16 v[60:63], v[252:255], v[188:191], v[60:63]
	buffer_load_dwordx4 v125, s[36:39], s51 offen lds
	v_pk_max_i16 v42, v42, 0
	v_mfma_f32_16x16x32_bf16 v[56:59], v[248:251], v[188:191], v[56:59]
	v_pk_max_i16 v43, v43, 0
	ds_read_b128 v[248:251], v121 offset:22528
	ds_read_b128 v[252:255], v121 offset:23552
	s_waitcnt lgkmcnt(6)
	v_mfma_f32_16x16x32_bf16 v[64:67], v[224:227], v[192:195], v[64:67]
	v_pk_max_i16 v44, v44, 0
	v_mfma_f32_16x16x32_bf16 v[68:71], v[228:231], v[192:195], v[68:71]
	s_mov_b32 m0, s34
	s_add_i32 s51, s50, 0x3e000
	v_pk_max_i16 v45, v45, 0
	v_mfma_f32_16x16x32_bf16 v[60:63], v[228:231], v[196:199], v[60:63]
	buffer_load_dwordx4 v125, s[36:39], s51 offen lds
	v_pk_max_i16 v46, v46, 0
	v_mfma_f32_16x16x32_bf16 v[56:59], v[224:227], v[196:199], v[56:59]
	v_pk_max_i16 v47, v47, 0
	ds_read_b128 v[224:227], v121 offset:24576
	ds_read_b128 v[228:231], v121 offset:25600
	s_waitcnt lgkmcnt(6)
	v_mfma_f32_16x16x32_bf16 v[64:67], v[232:235], v[200:203], v[64:67]
	ds_read_b128 v[80:83], v183 offset:1920
	ds_read_b128 v[84:87], v183 offset:1920
	ds_read_b128 v[76:79], v183 offset:1984
	ds_read_b128 v[72:75], v183 offset:1984
	v_mfma_f32_16x16x32_bf16 v[68:71], v[236:239], v[200:203], v[68:71]
	v_mfma_f32_16x16x32_bf16 v[60:63], v[236:239], v[204:207], v[60:63]
	v_mfma_f32_16x16x32_bf16 v[56:59], v[232:235], v[204:207], v[56:59]
	ds_read_b128 v[232:235], v121 offset:26624
	ds_read_b128 v[236:239], v121 offset:27648
	s_waitcnt lgkmcnt(10)
	v_mfma_f32_16x16x32_bf16 v[64:67], v[240:243], v[208:211], v[64:67]
	v_mfma_f32_16x16x32_bf16 v[68:71], v[244:247], v[208:211], v[68:71]
	v_mfma_f32_16x16x32_bf16 v[60:63], v[244:247], v[212:215], v[60:63]
	v_mfma_f32_16x16x32_bf16 v[56:59], v[240:243], v[212:215], v[56:59]
	ds_read_b128 v[240:243], v121 offset:28672
	ds_read_b128 v[244:247], v121 offset:29696
	s_waitcnt lgkmcnt(10)
	v_mfma_f32_16x16x32_bf16 v[64:67], v[248:251], v[216:219], v[64:67]
	v_mfma_f32_16x16x32_bf16 v[68:71], v[252:255], v[216:219], v[68:71]
	v_mfma_f32_16x16x32_bf16 v[60:63], v[252:255], v[220:223], v[60:63]
	v_mfma_f32_16x16x32_bf16 v[56:59], v[248:251], v[220:223], v[56:59]
	ds_read_b128 v[248:251], v121 offset:30720
	ds_read_b128 v[252:255], v121 offset:31744
	s_waitcnt lgkmcnt(6)
	v_mfma_f32_16x16x32_bf16 v[80:83], v[224:227], v[88:91], v[80:83]
	v_mfma_f32_16x16x32_bf16 v[76:79], v[228:231], v[88:91], v[76:79]
	v_mfma_f32_16x16x32_bf16 v[72:75], v[228:231], v[92:95], v[72:75]
	v_mfma_f32_16x16x32_bf16 v[84:87], v[224:227], v[92:95], v[84:87]
	ds_read_b128 v[224:227], v121 offset:32768
	ds_read_b128 v[228:231], v121 offset:33792
	s_waitcnt lgkmcnt(6)
	v_mfma_f32_16x16x32_bf16 v[80:83], v[232:235], v[96:99], v[80:83]
	v_cvt_pk_bf16_f32 v48, v64, v65
	v_mfma_f32_16x16x32_bf16 v[76:79], v[236:239], v[96:99], v[76:79]
	v_cvt_pk_bf16_f32 v49, v66, v67
	v_mfma_f32_16x16x32_bf16 v[72:75], v[236:239], v[100:103], v[72:75]
	v_cvt_pk_bf16_f32 v50, v68, v69
	v_mfma_f32_16x16x32_bf16 v[84:87], v[232:235], v[100:103], v[84:87]
	v_cvt_pk_bf16_f32 v51, v70, v71
	ds_read_b128 v[232:235], v121 offset:34816
	ds_read_b128 v[236:239], v121 offset:35840
	s_waitcnt lgkmcnt(6)
	v_mfma_f32_16x16x32_bf16 v[80:83], v[240:243], v[104:107], v[80:83]
	v_cvt_pk_bf16_f32 v52, v56, v57
	v_mfma_f32_16x16x32_bf16 v[76:79], v[244:247], v[104:107], v[76:79]
	v_cvt_pk_bf16_f32 v53, v58, v59
	v_mfma_f32_16x16x32_bf16 v[72:75], v[244:247], v[108:111], v[72:75]
	v_cvt_pk_bf16_f32 v54, v60, v61
	v_mfma_f32_16x16x32_bf16 v[84:87], v[240:243], v[108:111], v[84:87]
	v_cvt_pk_bf16_f32 v55, v62, v63
	ds_read_b128 v[240:243], v121 offset:36864
	ds_read_b128 v[244:247], v121 offset:37888
	s_waitcnt lgkmcnt(6)
	v_mfma_f32_16x16x32_bf16 v[80:83], v[248:251], v[184:187], v[80:83]
	v_pk_max_i16 v48, v48, 0
	v_mfma_f32_16x16x32_bf16 v[76:79], v[252:255], v[184:187], v[76:79]
	v_pk_max_i16 v49, v49, 0
	v_mfma_f32_16x16x32_bf16 v[72:75], v[252:255], v[188:191], v[72:75]
	v_pk_max_i16 v50, v50, 0
	v_mfma_f32_16x16x32_bf16 v[84:87], v[248:251], v[188:191], v[84:87]
	v_pk_max_i16 v51, v51, 0
	ds_read_b128 v[248:251], v121 offset:38912
	ds_read_b128 v[252:255], v121 offset:39936
	s_waitcnt lgkmcnt(6)
	v_mfma_f32_16x16x32_bf16 v[80:83], v[224:227], v[192:195], v[80:83]
	v_pk_max_i16 v52, v52, 0
	v_mfma_f32_16x16x32_bf16 v[76:79], v[228:231], v[192:195], v[76:79]
	v_pk_max_i16 v53, v53, 0
	v_mfma_f32_16x16x32_bf16 v[72:75], v[228:231], v[196:199], v[72:75]
	v_pk_max_i16 v54, v54, 0
	v_mfma_f32_16x16x32_bf16 v[84:87], v[224:227], v[196:199], v[84:87]
	v_pk_max_i16 v55, v55, 0
	s_waitcnt lgkmcnt(4)
	v_mfma_f32_16x16x32_bf16 v[80:83], v[232:235], v[200:203], v[80:83]
	ds_read_b128 v[64:67], v183 offset:2048
	ds_read_b128 v[56:59], v183 offset:2048
	ds_read_b128 v[68:71], v183 offset:2112
	ds_read_b128 v[60:63], v183 offset:2112
	v_mfma_f32_16x16x32_bf16 v[76:79], v[236:239], v[200:203], v[76:79]
	v_mfma_f32_16x16x32_bf16 v[72:75], v[236:239], v[204:207], v[72:75]
	v_mfma_f32_16x16x32_bf16 v[84:87], v[232:235], v[204:207], v[84:87]
	s_add_i32 s50, s50, 0x40000
	v_add_u32_e32 v183, 0x800, v183
	s_add_i32 s52, s52, 1
	s_cmp_eq_u32 s52, 3
	s_cbranch_scc0 .Lnerf_hid_b0
	s_waitcnt lgkmcnt(0)
	v_mfma_f32_16x16x32_bf16 v[80:83], v[240:243], v[208:211], v[80:83]
	v_mfma_f32_16x16x32_bf16 v[76:79], v[244:247], v[208:211], v[76:79]
	v_mfma_f32_16x16x32_bf16 v[72:75], v[244:247], v[212:215], v[72:75]
	v_mfma_f32_16x16x32_bf16 v[84:87], v[240:243], v[212:215], v[84:87]
	v_mfma_f32_16x16x32_bf16 v[80:83], v[248:251], v[216:219], v[80:83]
	v_mfma_f32_16x16x32_bf16 v[76:79], v[252:255], v[216:219], v[76:79]
	v_mfma_f32_16x16x32_bf16 v[72:75], v[252:255], v[220:223], v[72:75]
	v_mfma_f32_16x16x32_bf16 v[84:87], v[248:251], v[220:223], v[84:87]
	s_nop 7
	s_nop 1
	v_mov_b32_e32 v60, v84
	v_mov_b32_e32 v61, v85
	v_mov_b32_e32 v62, v86
	v_mov_b32_e32 v63, v87
	s_movk_i32 s20, 0x1800
	s_mov_b32 s21, 26
	s_waitcnt vmcnt(0)
	s_waitcnt vmcnt(0)
	s_barrier
	ds_read_b128 v[84:87], v121 offset:40960
	ds_read_b128 v[88:91], v121 offset:41984
	ds_read_b128 v[92:95], v121 offset:43008
	ds_read_b128 v[96:99], v121 offset:44032
	s_lshl_b32 s25, s21, 15
	s_add_i32 s24, s21, 1
	v_cvt_pk_bf16_f32 v56, v80, v81
	v_cvt_pk_bf16_f32 v57, v82, v83
	v_cvt_pk_bf16_f32 v58, v76, v77
	v_cvt_pk_bf16_f32 v59, v78, v79
	v_cvt_pk_bf16_f32 v60, v60, v61
	v_cvt_pk_bf16_f32 v61, v62, v63
	v_cvt_pk_bf16_f32 v62, v72, v73
	v_cvt_pk_bf16_f32 v63, v74, v75
	v_pk_max_i16 v56, v56, 0
	v_pk_max_i16 v57, v57, 0
	v_pk_max_i16 v58, v58, 0
	v_pk_max_i16 v59, v59, 0
	v_pk_max_i16 v60, v60, 0
	v_pk_max_i16 v61, v61, 0
	v_pk_max_i16 v62, v62, 0
	v_pk_max_i16 v63, v63, 0
	v_add_u32_e32 v104, s20, v131
	s_waitcnt lgkmcnt(2)
	v_mfma_f32_16x16x32_bf16 v[76:79], v[88:91], v[0:3], v[68:71]
	s_or_b32 s46, s25, 0x6000
	s_or_b32 s47, s25, 0x4000
	s_or_b32 s48, s25, 0x2000
	v_mfma_f32_16x16x32_bf16 v[68:71], v[88:91], v[4:7], v[68:71]
	ds_read_b128 v[80:83], v121 offset:45056
	ds_read_b128 v[88:91], v121 offset:46080
	ds_read_b128 v[100:103], v104 offset:128
	ds_read_b128 v[106:109], v104 offset:192
	v_mfma_f32_16x16x32_bf16 v[72:75], v[84:87], v[0:3], v[64:67]
	v_mfma_f32_16x16x32_bf16 v[64:67], v[84:87], v[4:7], v[64:67]
	s_mov_b32 m0, s35
	s_waitcnt lgkmcnt(4)
	v_mfma_f32_16x16x32_bf16 v[76:79], v[96:99], v[12:15], v[76:79]
	v_mfma_f32_16x16x32_bf16 v[68:71], v[96:99], v[8:11], v[68:71]
	ds_read_b128 v[84:87], v121 offset:47104
	ds_read_b128 v[96:99], v121 offset:48128
	buffer_load_dwordx4 v125, s[36:39], s25 offen lds
	v_mfma_f32_16x16x32_bf16 v[72:75], v[92:95], v[12:15], v[72:75]
	v_mfma_f32_16x16x32_bf16 v[64:67], v[92:95], v[8:11], v[64:67]
	s_mov_b32 m0, s42
	s_waitcnt lgkmcnt(4)
	v_mfma_f32_16x16x32_bf16 v[76:79], v[88:91], v[16:19], v[76:79]
	v_mfma_f32_16x16x32_bf16 v[68:71], v[88:91], v[20:23], v[68:71]
	ds_read_b128 v[88:91], v121 offset:49152
	ds_read_b128 v[92:95], v121 offset:50176
	buffer_load_dwordx4 v125, s[36:39], s48 offen lds
	v_mfma_f32_16x16x32_bf16 v[72:75], v[80:83], v[16:19], v[72:75]
	v_mfma_f32_16x16x32_bf16 v[64:67], v[80:83], v[20:23], v[64:67]
	s_mov_b32 m0, s41
	s_waitcnt lgkmcnt(2)
	v_mfma_f32_16x16x32_bf16 v[76:79], v[96:99], v[24:27], v[76:79]
	v_mfma_f32_16x16x32_bf16 v[68:71], v[96:99], v[28:31], v[68:71]
	ds_read_b128 v[80:83], v121 offset:51200
	ds_read_b128 v[96:99], v121 offset:52224
	buffer_load_dwordx4 v125, s[36:39], s47 offen lds
	v_mfma_f32_16x16x32_bf16 v[72:75], v[84:87], v[24:27], v[72:75]
	v_mfma_f32_16x16x32_bf16 v[64:67], v[84:87], v[28:31], v[64:67]
	s_mov_b32 m0, s40
	s_waitcnt lgkmcnt(2)
	v_mfma_f32_16x16x32_bf16 v[76:79], v[92:95], v[32:35], v[76:79]
	v_mfma_f32_16x16x32_bf16 v[68:71], v[92:95], v[36:39], v[68:71]
	ds_read_b128 v[84:87], v121 offset:53248
	ds_read_b128 v[92:95], v121 offset:54272
	buffer_load_dwordx4 v125, s[36:39], s46 offen lds
	v_mfma_f32_16x16x32_bf16 v[72:75], v[88:91], v[32:35], v[72:75]
	v_mfma_f32_16x16x32_bf16 v[64:67], v[88:91], v[36:39], v[64:67]
	s_waitcnt lgkmcnt(2)
	v_mfma_f32_16x16x32_bf16 v[76:79], v[96:99], v[40:43], v[76:79]
	v_mfma_f32_16x16x32_bf16 v[68:71], v[96:99], v[44:47], v[68:71]
	ds_read_b128 v[88:91], v121 offset:55296
	ds_read_b128 v[96:99], v121 offset:56320
	v_mfma_f32_16x16x32_bf16 v[72:75], v[80:83], v[40:43], v[72:75]
	v_mfma_f32_16x16x32_bf16 v[64:67], v[80:83], v[44:47], v[64:67]
	s_waitcnt lgkmcnt(2)
	v_mfma_f32_16x16x32_bf16 v[76:79], v[92:95], v[48:51], v[76:79]
	v_mfma_f32_16x16x32_bf16 v[68:71], v[92:95], v[52:55], v[68:71]
	ds_read_b128 v[80:83], v121 offset:57344
	ds_read_b128 v[92:95], v121 offset:58368
	v_mfma_f32_16x16x32_bf16 v[72:75], v[84:87], v[48:51], v[72:75]
	v_mfma_f32_16x16x32_bf16 v[64:67], v[84:87], v[52:55], v[64:67]
	s_waitcnt lgkmcnt(2)
	v_mfma_f32_16x16x32_bf16 v[76:79], v[96:99], v[56:59], v[76:79]
	v_mfma_f32_16x16x32_bf16 v[84:87], v[96:99], v[60:63], v[68:71]
	s_nop 2
	ds_read_b128 v[68:71], v121 offset:59392
	ds_read_b128 v[96:99], v121 offset:60416
	v_mfma_f32_16x16x32_bf16 v[72:75], v[88:91], v[56:59], v[72:75]
	v_mfma_f32_16x16x32_bf16 v[88:91], v[88:91], v[60:63], v[64:67]
	s_waitcnt lgkmcnt(2)
	v_mfma_f32_16x16x32_bf16 v[110:113], v[92:95], v[0:3], v[106:109]
	v_mfma_f32_16x16x32_bf16 v[92:95], v[92:95], v[4:7], v[106:109]
	s_nop 2
	ds_read_b128 v[106:109], v121 offset:61440
	ds_read_b128 v[114:117], v121 offset:62464
	v_mfma_f32_16x16x32_bf16 v[64:67], v[80:83], v[0:3], v[100:103]
	v_mfma_f32_16x16x32_bf16 v[80:83], v[80:83], v[4:7], v[100:103]
	s_nop 2
	ds_read_b128 v[100:103], v121 offset:63488
	ds_read_b128 v[184:187], v121 offset:64512
	s_waitcnt lgkmcnt(5)
	v_mfma_f32_16x16x32_bf16 v[188:191], v[68:71], v[12:15], v[64:67]
	v_cvt_pk_bf16_f32 v88, v88, v89
	s_nop 1
	v_cvt_pk_bf16_f32 v64, v72, v73
	v_cvt_pk_bf16_f32 v65, v74, v75
	v_cvt_pk_bf16_f32 v66, v76, v77
	v_cvt_pk_bf16_f32 v67, v78, v79
	v_mfma_f32_16x16x32_bf16 v[76:79], v[68:71], v[8:11], v[80:83]
	v_cvt_pk_bf16_f32 v69, v90, v91
	v_cvt_pk_bf16_f32 v70, v84, v85
	v_cvt_pk_bf16_f32 v71, v86, v87
	v_pk_max_i16 v64, v64, 0
	s_waitcnt lgkmcnt(4)
	v_mfma_f32_16x16x32_bf16 v[72:75], v[96:99], v[12:15], v[110:113]
	v_pk_max_i16 v65, v65, 0
	v_pk_max_i16 v66, v66, 0
	v_pk_max_i16 v67, v67, 0
	v_mfma_f32_16x16x32_bf16 v[92:95], v[96:99], v[8:11], v[92:95]
	v_pk_max_i16 v68, v88, 0
	v_pk_max_i16 v69, v69, 0
	v_pk_max_i16 v70, v70, 0
	v_pk_max_i16 v71, v71, 0
	s_waitcnt lgkmcnt(2)
	v_mfma_f32_16x16x32_bf16 v[84:87], v[114:117], v[20:23], v[92:95]
	ds_read_b128 v[88:91], v126 offset:57344
	s_nop 1
	ds_read_b128 v[92:95], v126 offset:58368
	ds_read_b128 v[96:99], v104 offset:256
	ds_read_b128 v[110:113], v104 offset:320
	v_mfma_f32_16x16x32_bf16 v[80:83], v[106:109], v[16:19], v[188:191]
	v_mfma_f32_16x16x32_bf16 v[72:75], v[114:117], v[16:19], v[72:75]
	v_mfma_f32_16x16x32_bf16 v[76:79], v[106:109], v[20:23], v[76:79]
	ds_read_b128 v[106:109], v126 offset:59392
	ds_read_b128 v[114:117], v126 offset:60416
	s_waitcnt lgkmcnt(7)
	v_mfma_f32_16x16x32_bf16 v[80:83], v[100:103], v[24:27], v[80:83]
	s_waitcnt lgkmcnt(6)
	v_mfma_f32_16x16x32_bf16 v[72:75], v[184:187], v[24:27], v[72:75]
	v_mfma_f32_16x16x32_bf16 v[84:87], v[184:187], v[28:31], v[84:87]
	v_mfma_f32_16x16x32_bf16 v[76:79], v[100:103], v[28:31], v[76:79]
	s_waitcnt lgkmcnt(4)
	v_mfma_f32_16x16x32_bf16 v[72:75], v[92:95], v[32:35], v[72:75]
	v_mfma_f32_16x16x32_bf16 v[84:87], v[92:95], v[36:39], v[84:87]
	ds_read_b128 v[92:95], v126 offset:61440
	ds_read_b128 v[100:103], v126 offset:62464
	v_mfma_f32_16x16x32_bf16 v[80:83], v[88:91], v[32:35], v[80:83]
	v_mfma_f32_16x16x32_bf16 v[76:79], v[88:91], v[36:39], v[76:79]
	s_waitcnt lgkmcnt(2)
	v_mfma_f32_16x16x32_bf16 v[72:75], v[114:117], v[40:43], v[72:75]
	v_mfma_f32_16x16x32_bf16 v[84:87], v[114:117], v[44:47], v[84:87]
	ds_read_b128 v[88:91], v126 offset:63488
	ds_read_b128 v[114:117], v126 offset:64512
	v_mfma_f32_16x16x32_bf16 v[80:83], v[106:109], v[40:43], v[80:83]
	v_mfma_f32_16x16x32_bf16 v[76:79], v[106:109], v[44:47], v[76:79]
	s_waitcnt lgkmcnt(3)
	v_mfma_f32_16x16x32_bf16 v[80:83], v[92:95], v[48:51], v[80:83]
	s_waitcnt lgkmcnt(2)
	v_mfma_f32_16x16x32_bf16 v[72:75], v[100:103], v[48:51], v[72:75]
	v_mfma_f32_16x16x32_bf16 v[84:87], v[100:103], v[52:55], v[84:87]
	v_mfma_f32_16x16x32_bf16 v[76:79], v[92:95], v[52:55], v[76:79]
	s_waitcnt lgkmcnt(1)
	v_mfma_f32_16x16x32_bf16 v[80:83], v[88:91], v[56:59], v[80:83]
	s_waitcnt lgkmcnt(0)
	v_mfma_f32_16x16x32_bf16 v[92:95], v[114:117], v[56:59], v[72:75]
	v_mfma_f32_16x16x32_bf16 v[84:87], v[114:117], v[60:63], v[84:87]
	v_mfma_f32_16x16x32_bf16 v[76:79], v[88:91], v[60:63], v[76:79]
	s_waitcnt vmcnt(0)
	s_waitcnt vmcnt(0)
	s_barrier
	ds_read_b128 v[88:91], v121 offset:8192
	ds_read_b128 v[100:103], v121 offset:9216
	ds_read_b128 v[106:109], v121 offset:10240
	ds_read_b128 v[114:117], v121 offset:11264
	s_cmp_lg_u32 s21, 29
	s_cselect_b32 s20, s24, 0
	s_add_i32 s21, s20, 1
	s_lshl_b32 s24, s20, 15
	v_cvt_pk_bf16_f32 v72, v80, v81
	v_cvt_pk_bf16_f32 v73, v82, v83
	v_cvt_pk_bf16_f32 v74, v92, v93
	v_cvt_pk_bf16_f32 v75, v94, v95
	v_cvt_pk_bf16_f32 v76, v76, v77
	v_cvt_pk_bf16_f32 v77, v78, v79
	v_cvt_pk_bf16_f32 v78, v84, v85
	v_cvt_pk_bf16_f32 v79, v86, v87
	v_pk_max_i16 v72, v72, 0
	v_pk_max_i16 v73, v73, 0
	v_pk_max_i16 v74, v74, 0
	v_pk_max_i16 v75, v75, 0
	v_pk_max_i16 v76, v76, 0
	v_pk_max_i16 v77, v77, 0
	v_pk_max_i16 v78, v78, 0
	v_pk_max_i16 v79, v79, 0
	s_waitcnt lgkmcnt(2)
	v_mfma_f32_16x16x32_bf16 v[84:87], v[100:103], v[0:3], v[110:113]
	s_or_b32 s46, s24, 0x4000
	s_or_b32 s25, s24, 0x6000
	s_or_b32 s47, s24, 0x2000
	v_mfma_f32_16x16x32_bf16 v[92:95], v[100:103], v[4:7], v[110:113]
	ds_read_b128 v[100:103], v121 offset:12288
	s_nop 1
	ds_read_b128 v[110:113], v121 offset:13312
	ds_read_b128 v[184:187], v104 offset:384
	ds_read_b128 v[188:191], v104 offset:448
	v_mfma_f32_16x16x32_bf16 v[80:83], v[88:91], v[0:3], v[96:99]
	v_mfma_f32_16x16x32_bf16 v[88:91], v[88:91], v[4:7], v[96:99]
	s_mov_b32 m0, s28
	s_waitcnt lgkmcnt(4)
	v_mfma_f32_16x16x32_bf16 v[84:87], v[114:117], v[12:15], v[84:87]
	v_mfma_f32_16x16x32_bf16 v[92:95], v[114:117], v[8:11], v[92:95]
	ds_read_b128 v[96:99], v121 offset:14336
	ds_read_b128 v[114:117], v121 offset:15360
	buffer_load_dwordx4 v125, s[36:39], s24 offen lds
	v_mfma_f32_16x16x32_bf16 v[80:83], v[106:109], v[12:15], v[80:83]
	v_mfma_f32_16x16x32_bf16 v[88:91], v[106:109], v[8:11], v[88:91]
	s_mov_b32 m0, s29
	s_waitcnt lgkmcnt(4)
	v_mfma_f32_16x16x32_bf16 v[84:87], v[110:113], v[16:19], v[84:87]
	v_mfma_f32_16x16x32_bf16 v[92:95], v[110:113], v[20:23], v[92:95]
	ds_read_b128 v[106:109], v121 offset:16384
	ds_read_b128 v[110:113], v121 offset:17408
	buffer_load_dwordx4 v125, s[36:39], s47 offen lds
	v_mfma_f32_16x16x32_bf16 v[80:83], v[100:103], v[16:19], v[80:83]
	v_mfma_f32_16x16x32_bf16 v[88:91], v[100:103], v[20:23], v[88:91]
	s_mov_b32 m0, s33
	s_waitcnt lgkmcnt(2)
	v_mfma_f32_16x16x32_bf16 v[84:87], v[114:117], v[24:27], v[84:87]
	v_mfma_f32_16x16x32_bf16 v[92:95], v[114:117], v[28:31], v[92:95]
	ds_read_b128 v[100:103], v121 offset:18432
	ds_read_b128 v[114:117], v121 offset:19456
	buffer_load_dwordx4 v125, s[36:39], s46 offen lds
	v_mfma_f32_16x16x32_bf16 v[80:83], v[96:99], v[24:27], v[80:83]
	v_mfma_f32_16x16x32_bf16 v[88:91], v[96:99], v[28:31], v[88:91]
	s_mov_b32 m0, s34
	s_waitcnt lgkmcnt(2)
	v_mfma_f32_16x16x32_bf16 v[84:87], v[110:113], v[32:35], v[84:87]
	v_mfma_f32_16x16x32_bf16 v[92:95], v[110:113], v[36:39], v[92:95]
	ds_read_b128 v[96:99], v121 offset:20480
	ds_read_b128 v[110:113], v121 offset:21504
	buffer_load_dwordx4 v125, s[36:39], s25 offen lds
	v_mfma_f32_16x16x32_bf16 v[80:83], v[106:109], v[32:35], v[80:83]
	v_mfma_f32_16x16x32_bf16 v[88:91], v[106:109], v[36:39], v[88:91]
	s_waitcnt lgkmcnt(2)
	v_mfma_f32_16x16x32_bf16 v[84:87], v[114:117], v[40:43], v[84:87]
	v_mfma_f32_16x16x32_bf16 v[92:95], v[114:117], v[44:47], v[92:95]
	ds_read_b128 v[106:109], v121 offset:22528
	ds_read_b128 v[114:117], v121 offset:23552
	v_mfma_f32_16x16x32_bf16 v[80:83], v[100:103], v[40:43], v[80:83]
	v_mfma_f32_16x16x32_bf16 v[88:91], v[100:103], v[44:47], v[88:91]
	s_waitcnt lgkmcnt(2)
	v_mfma_f32_16x16x32_bf16 v[84:87], v[110:113], v[48:51], v[84:87]
	v_mfma_f32_16x16x32_bf16 v[92:95], v[110:113], v[52:55], v[92:95]
	ds_read_b128 v[100:103], v121 offset:24576
	ds_read_b128 v[110:113], v121 offset:25600
	v_mfma_f32_16x16x32_bf16 v[80:83], v[96:99], v[48:51], v[80:83]
	v_mfma_f32_16x16x32_bf16 v[88:91], v[96:99], v[52:55], v[88:91]
	s_waitcnt lgkmcnt(2)
	v_mfma_f32_16x16x32_bf16 v[84:87], v[114:117], v[56:59], v[84:87]
	v_mfma_f32_16x16x32_bf16 v[92:95], v[114:117], v[60:63], v[92:95]
	ds_read_b128 v[96:99], v121 offset:26624
	ds_read_b128 v[114:117], v121 offset:27648
	v_mfma_f32_16x16x32_bf16 v[80:83], v[106:109], v[56:59], v[80:83]
	v_mfma_f32_16x16x32_bf16 v[88:91], v[106:109], v[60:63], v[88:91]
	s_waitcnt lgkmcnt(2)
	v_mfma_f32_16x16x32_bf16 v[192:195], v[110:113], v[0:3], v[188:191]
	v_mfma_f32_16x16x32_bf16 v[110:113], v[110:113], v[4:7], v[188:191]
	s_nop 2
	ds_read_b128 v[188:191], v121 offset:28672
	ds_read_b128 v[196:199], v121 offset:29696
	v_mfma_f32_16x16x32_bf16 v[106:109], v[100:103], v[0:3], v[184:187]
	v_mfma_f32_16x16x32_bf16 v[100:103], v[100:103], v[4:7], v[184:187]
	s_nop 2
	ds_read_b128 v[184:187], v121 offset:30720
	ds_read_b128 v[200:203], v121 offset:31744
	v_cvt_pk_bf16_f32 v80, v80, v81
	v_cvt_pk_bf16_f32 v81, v82, v83
	v_cvt_pk_bf16_f32 v82, v84, v85
	v_cvt_pk_bf16_f32 v83, v86, v87
	v_cvt_pk_bf16_f32 v84, v88, v89
	v_cvt_pk_bf16_f32 v85, v90, v91
	v_cvt_pk_bf16_f32 v86, v92, v93
	v_cvt_pk_bf16_f32 v87, v94, v95
	s_waitcnt lgkmcnt(5)
	v_mfma_f32_16x16x32_bf16 v[106:109], v[96:99], v[12:15], v[106:109]
	v_pk_max_i16 v80, v80, 0
	v_pk_max_i16 v81, v81, 0
	v_pk_max_i16 v82, v82, 0
	s_waitcnt lgkmcnt(4)
	v_mfma_f32_16x16x32_bf16 v[192:195], v[114:117], v[12:15], v[192:195]
	v_pk_max_i16 v83, v83, 0
	v_pk_max_i16 v84, v84, 0
	v_pk_max_i16 v85, v85, 0
	v_mfma_f32_16x16x32_bf16 v[110:113], v[114:117], v[8:11], v[110:113]
	v_pk_max_i16 v86, v86, 0
	v_pk_max_i16 v87, v87, 0
	v_mfma_f32_16x16x32_bf16 v[96:99], v[96:99], v[8:11], v[100:103]
	s_waitcnt lgkmcnt(3)
	v_mfma_f32_16x16x32_bf16 v[88:91], v[188:191], v[16:19], v[106:109]
	s_waitcnt lgkmcnt(2)
	v_mfma_f32_16x16x32_bf16 v[92:95], v[196:199], v[16:19], v[192:195]
	v_mfma_f32_16x16x32_bf16 v[100:103], v[196:199], v[20:23], v[110:113]
	ds_read_b128 v[106:109], v121 offset:32768
	s_nop 1
	ds_read_b128 v[110:113], v121 offset:33792
	ds_read_b128 v[114:117], v104 offset:512
	ds_read_b128 v[192:195], v104 offset:576
	v_mfma_f32_16x16x32_bf16 v[96:99], v[188:191], v[20:23], v[96:99]
	ds_read_b128 v[188:191], v121 offset:34816
	ds_read_b128 v[196:199], v121 offset:35840
	s_waitcnt lgkmcnt(7)
	v_mfma_f32_16x16x32_bf16 v[88:91], v[184:187], v[24:27], v[88:91]
	s_waitcnt lgkmcnt(6)
	v_mfma_f32_16x16x32_bf16 v[92:95], v[200:203], v[24:27], v[92:95]
	v_mfma_f32_16x16x32_bf16 v[100:103], v[200:203], v[28:31], v[100:103]
	v_mfma_f32_16x16x32_bf16 v[96:99], v[184:187], v[28:31], v[96:99]
	s_waitcnt lgkmcnt(4)
	v_mfma_f32_16x16x32_bf16 v[92:95], v[110:113], v[32:35], v[92:95]
	v_mfma_f32_16x16x32_bf16 v[100:103], v[110:113], v[36:39], v[100:103]
	ds_read_b128 v[110:113], v121 offset:36864
	ds_read_b128 v[184:187], v121 offset:37888
	v_mfma_f32_16x16x32_bf16 v[88:91], v[106:109], v[32:35], v[88:91]
	v_mfma_f32_16x16x32_bf16 v[96:99], v[106:109], v[36:39], v[96:99]
	s_waitcnt lgkmcnt(2)
	v_mfma_f32_16x16x32_bf16 v[92:95], v[196:199], v[40:43], v[92:95]
	v_mfma_f32_16x16x32_bf16 v[100:103], v[196:199], v[44:47], v[100:103]
	ds_read_b128 v[106:109], v121 offset:38912
	ds_read_b128 v[196:199], v121 offset:39936
	v_mfma_f32_16x16x32_bf16 v[88:91], v[188:191], v[40:43], v[88:91]
	v_mfma_f32_16x16x32_bf16 v[96:99], v[188:191], v[44:47], v[96:99]
	s_waitcnt lgkmcnt(3)
	v_mfma_f32_16x16x32_bf16 v[88:91], v[110:113], v[48:51], v[88:91]
	s_waitcnt lgkmcnt(2)
	v_mfma_f32_16x16x32_bf16 v[92:95], v[184:187], v[48:51], v[92:95]
	v_mfma_f32_16x16x32_bf16 v[100:103], v[184:187], v[52:55], v[100:103]
	v_mfma_f32_16x16x32_bf16 v[96:99], v[110:113], v[52:55], v[96:99]
	s_waitcnt lgkmcnt(1)
	v_mfma_f32_16x16x32_bf16 v[88:91], v[106:109], v[56:59], v[88:91]
	s_waitcnt lgkmcnt(0)
	v_mfma_f32_16x16x32_bf16 v[92:95], v[196:199], v[56:59], v[92:95]
	v_mfma_f32_16x16x32_bf16 v[100:103], v[196:199], v[60:63], v[100:103]
	v_mfma_f32_16x16x32_bf16 v[96:99], v[106:109], v[60:63], v[96:99]
	s_waitcnt vmcnt(0)
	s_waitcnt vmcnt(0)
	s_barrier
	ds_read_b128 v[106:109], v121 offset:40960
	ds_read_b128 v[110:113], v121 offset:41984
	ds_read_b128 v[184:187], v121 offset:43008
	ds_read_b128 v[188:191], v121 offset:44032
	s_cmp_lg_u32 s20, 29
	s_cselect_b32 s20, s21, 0
	s_add_i32 s21, s20, 1
	s_lshl_b32 s24, s20, 15
	v_cvt_pk_bf16_f32 v88, v88, v89
	v_cvt_pk_bf16_f32 v89, v90, v91
	v_cvt_pk_bf16_f32 v90, v92, v93
	v_cvt_pk_bf16_f32 v91, v94, v95
	v_cvt_pk_bf16_f32 v92, v96, v97
	v_cvt_pk_bf16_f32 v93, v98, v99
	v_cvt_pk_bf16_f32 v94, v100, v101
	v_cvt_pk_bf16_f32 v95, v102, v103
	v_pk_max_i16 v88, v88, 0
	v_pk_max_i16 v89, v89, 0
	v_pk_max_i16 v90, v90, 0
	v_pk_max_i16 v91, v91, 0
	v_pk_max_i16 v92, v92, 0
	v_pk_max_i16 v93, v93, 0
	v_pk_max_i16 v94, v94, 0
	v_pk_max_i16 v95, v95, 0
	s_waitcnt lgkmcnt(2)
	v_mfma_f32_16x16x32_bf16 v[100:103], v[110:113], v[0:3], v[192:195]
	s_or_b32 s46, s24, 0x4000
	s_or_b32 s25, s24, 0x6000
	s_or_b32 s47, s24, 0x2000
	v_mfma_f32_16x16x32_bf16 v[110:113], v[110:113], v[4:7], v[192:195]
	s_nop 2
	ds_read_b128 v[192:195], v121 offset:45056
	ds_read_b128 v[196:199], v121 offset:46080
	ds_read_b128 v[200:203], v104 offset:640
	ds_read_b128 v[204:207], v104 offset:704
	v_mfma_f32_16x16x32_bf16 v[96:99], v[106:109], v[0:3], v[114:117]
	v_mfma_f32_16x16x32_bf16 v[106:109], v[106:109], v[4:7], v[114:117]
	s_mov_b32 m0, s35
	s_waitcnt lgkmcnt(4)
	v_mfma_f32_16x16x32_bf16 v[100:103], v[188:191], v[12:15], v[100:103]
	v_mfma_f32_16x16x32_bf16 v[110:113], v[188:191], v[8:11], v[110:113]
	ds_read_b128 v[114:117], v121 offset:47104
	ds_read_b128 v[188:191], v121 offset:48128
	buffer_load_dwordx4 v125, s[36:39], s24 offen lds
	v_mfma_f32_16x16x32_bf16 v[96:99], v[184:187], v[12:15], v[96:99]
	v_mfma_f32_16x16x32_bf16 v[106:109], v[184:187], v[8:11], v[106:109]
	s_mov_b32 m0, s42
	s_waitcnt lgkmcnt(4)
	v_mfma_f32_16x16x32_bf16 v[100:103], v[196:199], v[16:19], v[100:103]
	v_mfma_f32_16x16x32_bf16 v[110:113], v[196:199], v[20:23], v[110:113]
	ds_read_b128 v[184:187], v121 offset:49152
	ds_read_b128 v[196:199], v121 offset:50176
	buffer_load_dwordx4 v125, s[36:39], s47 offen lds
	v_mfma_f32_16x16x32_bf16 v[96:99], v[192:195], v[16:19], v[96:99]
	v_mfma_f32_16x16x32_bf16 v[106:109], v[192:195], v[20:23], v[106:109]
	s_mov_b32 m0, s41
	s_waitcnt lgkmcnt(2)
	v_mfma_f32_16x16x32_bf16 v[100:103], v[188:191], v[24:27], v[100:103]
	v_mfma_f32_16x16x32_bf16 v[110:113], v[188:191], v[28:31], v[110:113]
	ds_read_b128 v[188:191], v121 offset:51200
	ds_read_b128 v[192:195], v121 offset:52224
	buffer_load_dwordx4 v125, s[36:39], s46 offen lds
	v_mfma_f32_16x16x32_bf16 v[96:99], v[114:117], v[24:27], v[96:99]
	v_mfma_f32_16x16x32_bf16 v[106:109], v[114:117], v[28:31], v[106:109]
	s_mov_b32 m0, s40
	s_waitcnt lgkmcnt(2)
	v_mfma_f32_16x16x32_bf16 v[100:103], v[196:199], v[32:35], v[100:103]
	v_mfma_f32_16x16x32_bf16 v[110:113], v[196:199], v[36:39], v[110:113]
	ds_read_b128 v[114:117], v121 offset:53248
	ds_read_b128 v[196:199], v121 offset:54272
	buffer_load_dwordx4 v125, s[36:39], s25 offen lds
	v_mfma_f32_16x16x32_bf16 v[96:99], v[184:187], v[32:35], v[96:99]
	v_mfma_f32_16x16x32_bf16 v[106:109], v[184:187], v[36:39], v[106:109]
	s_waitcnt lgkmcnt(2)
	v_mfma_f32_16x16x32_bf16 v[100:103], v[192:195], v[40:43], v[100:103]
	v_mfma_f32_16x16x32_bf16 v[110:113], v[192:195], v[44:47], v[110:113]
	ds_read_b128 v[184:187], v121 offset:55296
	ds_read_b128 v[192:195], v121 offset:56320
	v_mfma_f32_16x16x32_bf16 v[96:99], v[188:191], v[40:43], v[96:99]
	v_mfma_f32_16x16x32_bf16 v[106:109], v[188:191], v[44:47], v[106:109]
	s_waitcnt lgkmcnt(2)
	v_mfma_f32_16x16x32_bf16 v[100:103], v[196:199], v[48:51], v[100:103]
	v_mfma_f32_16x16x32_bf16 v[110:113], v[196:199], v[52:55], v[110:113]
	ds_read_b128 v[188:191], v121 offset:57344
	ds_read_b128 v[196:199], v121 offset:58368
	v_mfma_f32_16x16x32_bf16 v[96:99], v[114:117], v[48:51], v[96:99]
	v_mfma_f32_16x16x32_bf16 v[106:109], v[114:117], v[52:55], v[106:109]
	s_waitcnt lgkmcnt(2)
	v_mfma_f32_16x16x32_bf16 v[100:103], v[192:195], v[56:59], v[100:103]
	v_mfma_f32_16x16x32_bf16 v[110:113], v[192:195], v[60:63], v[110:113]
	ds_read_b128 v[114:117], v121 offset:59392
	ds_read_b128 v[192:195], v121 offset:60416
	v_mfma_f32_16x16x32_bf16 v[96:99], v[184:187], v[56:59], v[96:99]
	v_mfma_f32_16x16x32_bf16 v[106:109], v[184:187], v[60:63], v[106:109]
	s_waitcnt lgkmcnt(2)
	v_mfma_f32_16x16x32_bf16 v[208:211], v[196:199], v[0:3], v[204:207]
	v_mfma_f32_16x16x32_bf16 v[196:199], v[196:199], v[4:7], v[204:207]
	s_nop 2
	ds_read_b128 v[204:207], v121 offset:61440
	ds_read_b128 v[212:215], v121 offset:62464
	v_mfma_f32_16x16x32_bf16 v[184:187], v[188:191], v[0:3], v[200:203]
	v_mfma_f32_16x16x32_bf16 v[188:191], v[188:191], v[4:7], v[200:203]
	s_nop 2
	ds_read_b128 v[200:203], v121 offset:63488
	ds_read_b128 v[216:219], v121 offset:64512
	v_cvt_pk_bf16_f32 v96, v96, v97
	v_cvt_pk_bf16_f32 v97, v98, v99
	v_cvt_pk_bf16_f32 v98, v100, v101
	v_cvt_pk_bf16_f32 v99, v102, v103
	v_cvt_pk_bf16_f32 v100, v106, v107
	v_cvt_pk_bf16_f32 v101, v108, v109
	v_cvt_pk_bf16_f32 v102, v110, v111
	v_cvt_pk_bf16_f32 v103, v112, v113
	s_waitcnt lgkmcnt(5)
	v_mfma_f32_16x16x32_bf16 v[184:187], v[114:117], v[12:15], v[184:187]
	v_pk_max_i16 v96, v96, 0
	v_pk_max_i16 v97, v97, 0
	v_pk_max_i16 v98, v98, 0
	s_waitcnt lgkmcnt(4)
	v_mfma_f32_16x16x32_bf16 v[208:211], v[192:195], v[12:15], v[208:211]
	v_pk_max_i16 v99, v99, 0
	v_pk_max_i16 v100, v100, 0
	v_pk_max_i16 v101, v101, 0
	v_mfma_f32_16x16x32_bf16 v[192:195], v[192:195], v[8:11], v[196:199]
	v_pk_max_i16 v102, v102, 0
	v_pk_max_i16 v103, v103, 0
	v_mfma_f32_16x16x32_bf16 v[114:117], v[114:117], v[8:11], v[188:191]
	s_waitcnt lgkmcnt(3)
	v_mfma_f32_16x16x32_bf16 v[106:109], v[204:207], v[16:19], v[184:187]
	s_waitcnt lgkmcnt(2)
	v_mfma_f32_16x16x32_bf16 v[110:113], v[212:215], v[16:19], v[208:211]
	v_mfma_f32_16x16x32_bf16 v[184:187], v[212:215], v[20:23], v[192:195]
	ds_read_b128 v[188:191], v126 offset:57344
	s_nop 1
	ds_read_b128 v[192:195], v126 offset:58368
	ds_read_b128 v[196:199], v104 offset:768
	ds_read_b128 v[208:211], v104 offset:832
	v_mfma_f32_16x16x32_bf16 v[114:117], v[204:207], v[20:23], v[114:117]
	ds_read_b128 v[204:207], v126 offset:59392
	ds_read_b128 v[212:215], v126 offset:60416
	s_waitcnt lgkmcnt(7)
	v_mfma_f32_16x16x32_bf16 v[106:109], v[200:203], v[24:27], v[106:109]
	s_waitcnt lgkmcnt(6)
	v_mfma_f32_16x16x32_bf16 v[110:113], v[216:219], v[24:27], v[110:113]
	v_mfma_f32_16x16x32_bf16 v[184:187], v[216:219], v[28:31], v[184:187]
	v_mfma_f32_16x16x32_bf16 v[114:117], v[200:203], v[28:31], v[114:117]
	s_waitcnt lgkmcnt(4)
	v_mfma_f32_16x16x32_bf16 v[110:113], v[192:195], v[32:35], v[110:113]
	v_mfma_f32_16x16x32_bf16 v[184:187], v[192:195], v[36:39], v[184:187]
	ds_read_b128 v[192:195], v126 offset:61440
	ds_read_b128 v[200:203], v126 offset:62464
	v_mfma_f32_16x16x32_bf16 v[106:109], v[188:191], v[32:35], v[106:109]
	v_mfma_f32_16x16x32_bf16 v[114:117], v[188:191], v[36:39], v[114:117]
	s_waitcnt lgkmcnt(2)
	v_mfma_f32_16x16x32_bf16 v[110:113], v[212:215], v[40:43], v[110:113]
	v_mfma_f32_16x16x32_bf16 v[184:187], v[212:215], v[44:47], v[184:187]
	ds_read_b128 v[188:191], v126 offset:63488
	ds_read_b128 v[212:215], v126 offset:64512
	v_mfma_f32_16x16x32_bf16 v[106:109], v[204:207], v[40:43], v[106:109]
	v_mfma_f32_16x16x32_bf16 v[114:117], v[204:207], v[44:47], v[114:117]
	s_waitcnt lgkmcnt(3)
	v_mfma_f32_16x16x32_bf16 v[106:109], v[192:195], v[48:51], v[106:109]
	s_waitcnt lgkmcnt(2)
	v_mfma_f32_16x16x32_bf16 v[110:113], v[200:203], v[48:51], v[110:113]
	v_mfma_f32_16x16x32_bf16 v[184:187], v[200:203], v[52:55], v[184:187]
	v_mfma_f32_16x16x32_bf16 v[114:117], v[192:195], v[52:55], v[114:117]
	s_waitcnt lgkmcnt(1)
	v_mfma_f32_16x16x32_bf16 v[106:109], v[188:191], v[56:59], v[106:109]
	s_waitcnt lgkmcnt(0)
	v_mfma_f32_16x16x32_bf16 v[110:113], v[212:215], v[56:59], v[110:113]
	v_mfma_f32_16x16x32_bf16 v[184:187], v[212:215], v[60:63], v[184:187]
	v_mfma_f32_16x16x32_bf16 v[114:117], v[188:191], v[60:63], v[114:117]
	s_waitcnt vmcnt(0)
	s_waitcnt vmcnt(0)
	s_barrier
	ds_read_b128 v[188:191], v121 offset:8192
	ds_read_b128 v[192:195], v121 offset:9216
	ds_read_b128 v[200:203], v121 offset:10240
	ds_read_b128 v[204:207], v121 offset:11264
	s_cmp_lg_u32 s20, 29
	s_cselect_b32 s46, s21, 0
	s_lshl_b32 s20, s46, 15
	v_cvt_pk_bf16_f32 v105, v106, v107
	v_pk_max_i16 v106, v105, 0
	v_cvt_pk_bf16_f32 v105, v108, v109
	v_pk_max_i16 v107, v105, 0
	v_cvt_pk_bf16_f32 v105, v110, v111
	v_pk_max_i16 v108, v105, 0
	v_cvt_pk_bf16_f32 v105, v112, v113
	v_pk_max_i16 v109, v105, 0
	v_cvt_pk_bf16_f32 v105, v114, v115
	v_pk_max_i16 v110, v105, 0
	v_cvt_pk_bf16_f32 v105, v116, v117
	v_pk_max_i16 v111, v105, 0
	v_cvt_pk_bf16_f32 v105, v184, v185
	v_pk_max_i16 v112, v105, 0
	v_cvt_pk_bf16_f32 v105, v186, v187
	v_pk_max_i16 v113, v105, 0
	s_waitcnt lgkmcnt(2)
	v_mfma_f32_16x16x32_bf16 v[184:187], v[192:195], v[0:3], v[208:211]
	v_mfma_f32_16x16x32_bf16 v[192:195], v[192:195], v[4:7], v[208:211]
	s_nop 2
	ds_read_b128 v[208:211], v121 offset:12288
	ds_read_b128 v[212:215], v121 offset:13312
	ds_read_b128 v[216:219], v104 offset:896
	ds_read_b128 v[220:223], v104 offset:960
	v_mfma_f32_16x16x32_bf16 v[114:117], v[188:191], v[0:3], v[196:199]
	v_mfma_f32_16x16x32_bf16 v[188:191], v[188:191], v[4:7], v[196:199]
	s_mov_b32 m0, s28
	s_waitcnt lgkmcnt(4)
	v_mfma_f32_16x16x32_bf16 v[184:187], v[204:207], v[12:15], v[184:187]
	v_mfma_f32_16x16x32_bf16 v[192:195], v[204:207], v[8:11], v[192:195]
	ds_read_b128 v[196:199], v121 offset:14336
	ds_read_b128 v[204:207], v121 offset:15360
	buffer_load_dwordx4 v125, s[36:39], s20 offen lds
	v_mfma_f32_16x16x32_bf16 v[114:117], v[200:203], v[12:15], v[114:117]
	v_mfma_f32_16x16x32_bf16 v[188:191], v[200:203], v[8:11], v[188:191]
	s_waitcnt lgkmcnt(4)
	v_mfma_f32_16x16x32_bf16 v[184:187], v[212:215], v[16:19], v[184:187]
	v_mfma_f32_16x16x32_bf16 v[192:195], v[212:215], v[20:23], v[192:195]
	ds_read_b128 v[200:203], v121 offset:16384
	ds_read_b128 v[212:215], v121 offset:17408
	v_mfma_f32_16x16x32_bf16 v[114:117], v[208:211], v[16:19], v[114:117]
	v_mfma_f32_16x16x32_bf16 v[188:191], v[208:211], v[20:23], v[188:191]
	s_waitcnt lgkmcnt(2)
	v_mfma_f32_16x16x32_bf16 v[184:187], v[204:207], v[24:27], v[184:187]
	v_mfma_f32_16x16x32_bf16 v[192:195], v[204:207], v[28:31], v[192:195]
	ds_read_b128 v[204:207], v121 offset:18432
	ds_read_b128 v[208:211], v121 offset:19456
	v_mfma_f32_16x16x32_bf16 v[114:117], v[196:199], v[24:27], v[114:117]
	v_mfma_f32_16x16x32_bf16 v[188:191], v[196:199], v[28:31], v[188:191]
	s_waitcnt lgkmcnt(2)
	v_mfma_f32_16x16x32_bf16 v[184:187], v[212:215], v[32:35], v[184:187]
	v_mfma_f32_16x16x32_bf16 v[192:195], v[212:215], v[36:39], v[192:195]
	ds_read_b128 v[196:199], v121 offset:20480
	ds_read_b128 v[212:215], v121 offset:21504
	v_mfma_f32_16x16x32_bf16 v[114:117], v[200:203], v[32:35], v[114:117]
	v_mfma_f32_16x16x32_bf16 v[188:191], v[200:203], v[36:39], v[188:191]
	s_waitcnt lgkmcnt(2)
	v_mfma_f32_16x16x32_bf16 v[184:187], v[208:211], v[40:43], v[184:187]
	v_mfma_f32_16x16x32_bf16 v[192:195], v[208:211], v[44:47], v[192:195]
	ds_read_b128 v[200:203], v121 offset:22528
	ds_read_b128 v[208:211], v121 offset:23552
	v_mfma_f32_16x16x32_bf16 v[114:117], v[204:207], v[40:43], v[114:117]
	v_mfma_f32_16x16x32_bf16 v[188:191], v[204:207], v[44:47], v[188:191]
	s_waitcnt lgkmcnt(2)
	v_mfma_f32_16x16x32_bf16 v[184:187], v[212:215], v[48:51], v[184:187]
	v_mfma_f32_16x16x32_bf16 v[192:195], v[212:215], v[52:55], v[192:195]
	ds_read_b128 v[204:207], v121 offset:24576
	ds_read_b128 v[212:215], v121 offset:25600
	v_mfma_f32_16x16x32_bf16 v[114:117], v[196:199], v[48:51], v[114:117]
	v_mfma_f32_16x16x32_bf16 v[188:191], v[196:199], v[52:55], v[188:191]
	s_waitcnt lgkmcnt(2)
	v_mfma_f32_16x16x32_bf16 v[184:187], v[208:211], v[56:59], v[184:187]
	v_mfma_f32_16x16x32_bf16 v[192:195], v[208:211], v[60:63], v[192:195]
	ds_read_b128 v[196:199], v121 offset:26624
	ds_read_b128 v[208:211], v121 offset:27648
	v_mfma_f32_16x16x32_bf16 v[114:117], v[200:203], v[56:59], v[114:117]
	v_mfma_f32_16x16x32_bf16 v[188:191], v[200:203], v[60:63], v[188:191]
	s_waitcnt lgkmcnt(3)
	v_mfma_f32_16x16x32_bf16 v[200:203], v[204:207], v[0:3], v[216:219]
	s_waitcnt lgkmcnt(2)
	v_mfma_f32_16x16x32_bf16 v[0:3], v[212:215], v[0:3], v[220:223]
	v_mfma_f32_16x16x32_bf16 v[212:215], v[212:215], v[4:7], v[220:223]
	s_nop 2
	ds_read_b128 v[220:223], v121 offset:28672
	ds_read_b128 v[224:227], v121 offset:29696
	v_mfma_f32_16x16x32_bf16 v[4:7], v[204:207], v[4:7], v[216:219]
	ds_read_b128 v[204:207], v121 offset:30720
	s_nop 1
	ds_read_b128 v[216:219], v121 offset:31744
	v_cvt_pk_bf16_f32 v105, v114, v115
	s_waitcnt lgkmcnt(4)
	v_mfma_f32_16x16x32_bf16 v[0:3], v[208:211], v[12:15], v[0:3]
	v_pk_max_i16 v114, v105, 0
	v_cvt_pk_bf16_f32 v105, v116, v117
	v_pk_max_i16 v115, v105, 0
	v_mfma_f32_16x16x32_bf16 v[4:7], v[196:199], v[8:11], v[4:7]
	v_cvt_pk_bf16_f32 v105, v186, v187
	v_pk_max_i16 v117, v105, 0
	v_cvt_pk_bf16_f32 v105, v188, v189
	v_mfma_f32_16x16x32_bf16 v[200:203], v[196:199], v[12:15], v[200:203]
	v_cvt_pk_bf16_f32 v12, v184, v185
	v_pk_max_i16 v116, v12, 0
	v_mfma_f32_16x16x32_bf16 v[12:15], v[208:211], v[8:11], v[212:215]
	v_cvt_pk_bf16_f32 v9, v190, v191
	v_cvt_pk_bf16_f32 v10, v192, v193
	v_cvt_pk_bf16_f32 v11, v194, v195
	v_pk_max_i16 v8, v105, 0
	v_pk_max_i16 v9, v9, 0
	v_pk_max_i16 v10, v10, 0
	v_pk_max_i16 v11, v11, 0
	s_waitcnt lgkmcnt(3)
	v_mfma_f32_16x16x32_bf16 v[184:187], v[220:223], v[16:19], v[200:203]
	s_waitcnt lgkmcnt(2)
	v_mfma_f32_16x16x32_bf16 v[0:3], v[224:227], v[16:19], v[0:3]
	ds_read_b128 v[16:19], v121 offset:32768
	ds_read_b128 v[188:191], v121 offset:33792
	ds_read_b128 v[192:195], v104 offset:1024
	v_mfma_f32_16x16x32_bf16 v[4:7], v[220:223], v[20:23], v[4:7]
	v_mfma_f32_16x16x32_bf16 v[12:15], v[224:227], v[20:23], v[12:15]
	s_waitcnt lgkmcnt(4)
	v_mfma_f32_16x16x32_bf16 v[20:23], v[204:207], v[24:27], v[184:187]
	s_waitcnt lgkmcnt(3)
	v_mfma_f32_16x16x32_bf16 v[0:3], v[216:219], v[24:27], v[0:3]
	ds_read_b128 v[24:27], v121 offset:34816
	ds_read_b128 v[184:187], v121 offset:35840
	v_mfma_f32_16x16x32_bf16 v[4:7], v[204:207], v[28:31], v[4:7]
	v_mfma_f32_16x16x32_bf16 v[12:15], v[216:219], v[28:31], v[12:15]
	s_waitcnt lgkmcnt(4)
	v_mfma_f32_16x16x32_bf16 v[20:23], v[16:19], v[32:35], v[20:23]
	s_waitcnt lgkmcnt(3)
	v_mfma_f32_16x16x32_bf16 v[0:3], v[188:191], v[32:35], v[0:3]
	ds_read_b128 v[28:31], v121 offset:36864
	ds_read_b128 v[32:35], v121 offset:37888
	v_mfma_f32_16x16x32_bf16 v[4:7], v[16:19], v[36:39], v[4:7]
	v_mfma_f32_16x16x32_bf16 v[12:15], v[188:191], v[36:39], v[12:15]
	s_waitcnt lgkmcnt(3)
	v_mfma_f32_16x16x32_bf16 v[16:19], v[24:27], v[40:43], v[20:23]
	s_nop 2
	ds_read_b128 v[20:23], v121 offset:38912
	ds_read_b128 v[36:39], v121 offset:39936
	s_waitcnt lgkmcnt(4)
	v_mfma_f32_16x16x32_bf16 v[0:3], v[184:187], v[40:43], v[0:3]
	v_mfma_f32_16x16x32_bf16 v[4:7], v[24:27], v[44:47], v[4:7]
	v_mfma_f32_16x16x32_bf16 v[12:15], v[184:187], v[44:47], v[12:15]
	s_waitcnt lgkmcnt(2)
	v_mfma_f32_16x16x32_bf16 v[0:3], v[32:35], v[48:51], v[0:3]
	v_mfma_f32_16x16x32_bf16 v[4:7], v[28:31], v[52:55], v[4:7]
	v_mfma_f32_16x16x32_bf16 v[16:19], v[28:31], v[48:51], v[16:19]
	v_mfma_f32_16x16x32_bf16 v[12:15], v[32:35], v[52:55], v[12:15]
	s_waitcnt lgkmcnt(0)
	v_mfma_f32_16x16x32_bf16 v[0:3], v[36:39], v[56:59], v[0:3]
	v_mfma_f32_16x16x32_bf16 v[4:7], v[20:23], v[60:63], v[4:7]
	v_mfma_f32_16x16x32_bf16 v[16:19], v[20:23], v[56:59], v[16:19]
	v_mfma_f32_16x16x32_bf16 v[12:15], v[36:39], v[60:63], v[12:15]
	s_waitcnt vmcnt(0)
	s_waitcnt vmcnt(0)
	s_barrier
	ds_read_b128 v[20:23], v121 offset:40960
	ds_read_b128 v[24:27], v121 offset:41984
	ds_read_b128 v[28:31], v121 offset:43008
	ds_read_b128 v[32:35], v121 offset:44032
	v_cvt_pk_bf16_f32 v0, v0, v1
	v_cvt_pk_bf16_f32 v16, v16, v17
	v_cvt_pk_bf16_f32 v17, v18, v19
	v_pk_max_i16 v18, v0, 0
	v_cvt_pk_bf16_f32 v0, v2, v3
	v_pk_max_i16 v19, v0, 0
	v_cvt_pk_bf16_f32 v0, v4, v5
	v_cvt_pk_bf16_f32 v1, v6, v7
	v_cvt_pk_bf16_f32 v2, v12, v13
	v_cvt_pk_bf16_f32 v3, v14, v15
	v_pk_max_i16 v0, v0, 0
	v_pk_max_i16 v1, v1, 0
	v_pk_max_i16 v2, v2, 0
	v_pk_max_i16 v3, v3, 0
	v_pk_max_i16 v16, v16, 0
	v_pk_max_i16 v17, v17, 0
	s_waitcnt lgkmcnt(3)
	v_mfma_f32_16x16x32_bf16 v[4:7], v[20:23], v[64:67], v[192:195]
	ds_read_b128 v[12:15], v121 offset:45056
	v_mfma_f32_16x16x32_bf16 v[20:23], v[20:23], v[68:71], v[192:195]
	s_waitcnt lgkmcnt(3)
	v_mfma_f32_16x16x32_bf16 v[4:7], v[24:27], v[72:75], v[4:7]
	ds_read_b128 v[36:39], v121 offset:46080
	v_mfma_f32_16x16x32_bf16 v[20:23], v[24:27], v[76:79], v[20:23]
	s_waitcnt lgkmcnt(3)
	v_mfma_f32_16x16x32_bf16 v[4:7], v[28:31], v[80:83], v[4:7]
	ds_read_b128 v[24:27], v121 offset:47104
	v_mfma_f32_16x16x32_bf16 v[20:23], v[28:31], v[84:87], v[20:23]
	s_waitcnt lgkmcnt(3)
	v_mfma_f32_16x16x32_bf16 v[4:7], v[32:35], v[88:91], v[4:7]
	ds_read_b128 v[28:31], v121 offset:48128
	v_mfma_f32_16x16x32_bf16 v[20:23], v[32:35], v[92:95], v[20:23]
	s_waitcnt lgkmcnt(3)
	v_mfma_f32_16x16x32_bf16 v[4:7], v[12:15], v[96:99], v[4:7]
	v_mfma_f32_16x16x32_bf16 v[12:15], v[12:15], v[100:103], v[20:23]
	s_waitcnt lgkmcnt(2)
	v_mfma_f32_16x16x32_bf16 v[4:7], v[36:39], v[106:109], v[4:7]
	v_mfma_f32_16x16x32_bf16 v[12:15], v[36:39], v[110:113], v[12:15]
	s_waitcnt lgkmcnt(1)
	v_mfma_f32_16x16x32_bf16 v[4:7], v[24:27], v[114:117], v[4:7]
	v_mfma_f32_16x16x32_bf16 v[8:11], v[24:27], v[8:11], v[12:15]
	s_waitcnt lgkmcnt(0)
	v_mfma_f32_16x16x32_bf16 v[4:7], v[28:31], v[16:19], v[4:7]
	v_mfma_f32_16x16x32_bf16 v[0:3], v[28:31], v[0:3], v[8:11]
	s_and_saveexec_b64 s[20:21], s[2:3]
	s_cbranch_execz .LBB1_20
	s_nop 4
	v_mul_f32_e32 v6, 0xbfb8aa3b, v6
	v_mul_f32_e32 v7, 0xbfb8aa3b, v7
	v_exp_f32_e32 v6, v6
	v_exp_f32_e32 v7, v7
	v_mul_f32_e32 v4, 0xbfb8aa3b, v4
	v_mul_f32_e32 v5, 0xbfb8aa3b, v5
	v_exp_f32_e32 v4, v4
	v_pk_add_f32 v[6:7], v[6:7], 1.0 op_sel_hi:[1,0]
	v_exp_f32_e32 v5, v5
	v_div_scale_f32 v8, s[24:25], v7, v7, 1.0
	v_rcp_f32_e32 v9, v8
	s_lshl_b32 s24, s45, 6
	s_add_i32 s47, s43, s24
	v_pk_add_f32 v[4:5], v[4:5], 1.0 op_sel_hi:[1,0]
	v_fma_f32 v10, -v8, v9, 1.0
	v_fmac_f32_e32 v9, v10, v9
	v_div_scale_f32 v10, vcc, 1.0, v7, 1.0
	v_mul_f32_e32 v11, v10, v9
	v_fma_f32 v12, -v8, v11, v10
	v_fmac_f32_e32 v11, v12, v9
	v_fma_f32 v8, -v8, v11, v10
	v_div_scale_f32 v10, s[24:25], v6, v6, 1.0
	v_rcp_f32_e32 v12, v10
	v_div_fmas_f32 v8, v8, v9, v11
	v_div_fixup_f32 v7, v8, v7, 1.0
	v_fma_f32 v8, -v10, v12, 1.0
	v_fmac_f32_e32 v12, v8, v12
	v_div_scale_f32 v8, vcc, 1.0, v6, 1.0
	v_mul_f32_e32 v9, v8, v12
	v_fma_f32 v11, -v10, v9, v8
	v_fmac_f32_e32 v9, v11, v12
	v_fma_f32 v8, -v10, v9, v8
	v_div_scale_f32 v10, s[24:25], v5, v5, 1.0
	v_rcp_f32_e32 v11, v10
	v_div_fmas_f32 v8, v8, v12, v9
	v_div_fixup_f32 v6, v8, v6, 1.0
	v_fma_f32 v8, -v10, v11, 1.0
	v_fmac_f32_e32 v11, v8, v11
	v_div_scale_f32 v8, vcc, 1.0, v5, 1.0
	v_mul_f32_e32 v9, v8, v11
	v_fma_f32 v12, -v10, v9, v8
	v_fmac_f32_e32 v9, v12, v11
	v_fma_f32 v8, -v10, v9, v8
	v_div_scale_f32 v10, s[24:25], v4, v4, 1.0
	v_rcp_f32_e32 v12, v10
	v_div_fmas_f32 v8, v8, v11, v9
	v_div_fixup_f32 v5, v8, v5, 1.0
	s_mov_b64 s[24:25], -1
	v_fma_f32 v8, -v10, v12, 1.0
	v_fmac_f32_e32 v12, v8, v12
	v_div_scale_f32 v8, vcc, 1.0, v4, 1.0
	v_mul_f32_e32 v9, v8, v12
	v_fma_f32 v11, -v10, v9, v8
	v_fmac_f32_e32 v9, v11, v12
	v_fma_f32 v8, -v10, v9, v8
	v_div_fmas_f32 v8, v8, v12, v9
	v_div_fixup_f32 v4, v8, v4, 1.0
	s_and_b64 vcc, exec, s[16:17]
	s_cbranch_vccz .LBB1_14
	v_or_b32_e32 v8, s47, v130
	v_lshl_add_u32 v8, v8, 4, v182
	ds_write_b128 v8, v[4:7]
	s_mov_b64 s[24:25], 0

	.amdhsa_kernel _Z9nerf_mainPKfS0_S0_PKiS2_PKcS0_Pf
		.amdhsa_group_segment_fixed_size 139264
		.amdhsa_private_segment_fixed_size 0
		.amdhsa_kernarg_size 64
		.amdhsa_user_sgpr_count 2
		.amdhsa_user_sgpr_dispatch_ptr 0
		.amdhsa_user_sgpr_queue_ptr 0
		.amdhsa_user_sgpr_kernarg_segment_ptr 1
		.amdhsa_user_sgpr_dispatch_id 0
		.amdhsa_user_sgpr_kernarg_preload_length 0
		.amdhsa_user_sgpr_kernarg_preload_offset 0
		.amdhsa_user_sgpr_private_segment_size 0
		.amdhsa_uses_dynamic_stack 0
		.amdhsa_enable_private_segment 0
		.amdhsa_system_sgpr_workgroup_id_x 1
		.amdhsa_system_sgpr_workgroup_id_y 0
		.amdhsa_system_sgpr_workgroup_id_z 0
		.amdhsa_system_sgpr_workgroup_info 0
		.amdhsa_system_vgpr_workitem_id 0
		.amdhsa_next_free_vgpr 256
		.amdhsa_next_free_sgpr 96
		.amdhsa_accum_offset 256
		.amdhsa_reserve_vcc 1
		.amdhsa_float_round_mode_32 0
		.amdhsa_float_round_mode_16_64 0
		.amdhsa_float_denorm_mode_32 3
		.amdhsa_float_denorm_mode_16_64 3
		.amdhsa_dx10_clamp 1
		.amdhsa_ieee_mode 1
		.amdhsa_fp16_overflow 0
		.amdhsa_tg_split 0
		.amdhsa_exception_fp_ieee_invalid_op 0
		.amdhsa_exception_fp_denorm_src 0
		.amdhsa_exception_fp_ieee_div_zero 0
		.amdhsa_exception_fp_ieee_overflow 0
		.amdhsa_exception_fp_ieee_underflow 0
		.amdhsa_exception_fp_ieee_inexact 0
		.amdhsa_exception_int_div_zero 0
	.end_amdhsa_kernel

.Lfunc_end1:
	.size	_Z9nerf_mainPKfS0_S0_PKiS2_PKcS0_Pf, .Lfunc_end1-_Z9nerf_mainPKfS0_S0_PKiS2_PKcS0_Pf
	.set _Z9nerf_mainPKfS0_S0_PKiS2_PKcS0_Pf.num_vgpr, 256
	.set _Z9nerf_mainPKfS0_S0_PKiS2_PKcS0_Pf.num_agpr, 0
	.set _Z9nerf_mainPKfS0_S0_PKiS2_PKcS0_Pf.numbered_sgpr, 49
	.set _Z9nerf_mainPKfS0_S0_PKiS2_PKcS0_Pf.num_named_barrier, 0
	.set _Z9nerf_mainPKfS0_S0_PKiS2_PKcS0_Pf.private_seg_size, 0
	.set _Z9nerf_mainPKfS0_S0_PKiS2_PKcS0_Pf.uses_vcc, 1
	.set _Z9nerf_mainPKfS0_S0_PKiS2_PKcS0_Pf.uses_flat_scratch, 0
	.set _Z9nerf_mainPKfS0_S0_PKiS2_PKcS0_Pf.has_dyn_sized_stack, 0
	.set _Z9nerf_mainPKfS0_S0_PKiS2_PKcS0_Pf.has_recursion, 0
	.set _Z9nerf_mainPKfS0_S0_PKiS2_PKcS0_Pf.has_indirect_call, 0

amdhsa.kernels:
  - .agpr_count:     0
    .args:
      - .actual_access:  read_only
        .address_space:  global
        .offset:         0
        .size:           8
        .value_kind:     global_buffer
      - .actual_access:  read_only
        .address_space:  global
        .offset:         8
        .size:           8
        .value_kind:     global_buffer
      - .actual_access:  read_only
        .address_space:  global
        .offset:         16
        .size:           8
        .value_kind:     global_buffer
      - .actual_access:  read_only
        .address_space:  global
        .offset:         24
        .size:           8
        .value_kind:     global_buffer
      - .actual_access:  read_only
        .address_space:  global
        .offset:         32
        .size:           8
        .value_kind:     global_buffer
      - .actual_access:  read_only
        .address_space:  global
        .offset:         40
        .size:           8
        .value_kind:     global_buffer
      - .actual_access:  read_only
        .address_space:  global
        .offset:         48
        .size:           8
        .value_kind:     global_buffer
      - .actual_access:  read_only
        .address_space:  global
        .offset:         56
        .size:           8
        .value_kind:     global_buffer
      - .actual_access:  read_only
        .address_space:  global
        .offset:         64
        .size:           8
        .value_kind:     global_buffer
      - .actual_access:  read_only
        .address_space:  global
        .offset:         72
        .size:           8
        .value_kind:     global_buffer
      - .actual_access:  read_only
        .address_space:  global
        .offset:         80
        .size:           8
        .value_kind:     global_buffer
      - .actual_access:  write_only
        .address_space:  global
        .offset:         88
        .size:           8
        .value_kind:     global_buffer
      - .actual_access:  write_only
        .address_space:  global
        .offset:         96
        .size:           8
        .value_kind:     global_buffer
    .group_segment_fixed_size: 0
    .kernarg_segment_align: 8
    .kernarg_segment_size: 104
    .language:       OpenCL C
    .language_version:
      - 2
      - 0
    .max_flat_workgroup_size: 256
    .name:           _Z9nerf_prepPKfS0_S0_S0_S0_S0_S0_S0_S0_S0_S0_PtPf
    .private_segment_fixed_size: 0
    .sgpr_count:     26
    .sgpr_spill_count: 0
    .symbol:         _Z9nerf_prepPKfS0_S0_S0_S0_S0_S0_S0_S0_S0_S0_PtPf.kd
    .uniform_work_group_size: 1
    .uses_dynamic_stack: false
    .vgpr_count:     54
    .vgpr_spill_count: 0
    .wavefront_size: 64
  - .agpr_count:     0
    .args:
      - .actual_access:  read_only
        .address_space:  global
        .offset:         0
        .size:           8
        .value_kind:     global_buffer
      - .actual_access:  read_only
        .address_space:  global
        .offset:         8
        .size:           8
        .value_kind:     global_buffer
      - .actual_access:  read_only
        .address_space:  global
        .offset:         16
        .size:           8
        .value_kind:     global_buffer
      - .actual_access:  read_only
        .address_space:  global
        .offset:         24
        .size:           8
        .value_kind:     global_buffer
      - .actual_access:  read_only
        .address_space:  global
        .offset:         32
        .size:           8
        .value_kind:     global_buffer
      - .actual_access:  read_only
        .address_space:  global
        .offset:         40
        .size:           8
        .value_kind:     global_buffer
      - .actual_access:  read_only
        .address_space:  global
        .offset:         48
        .size:           8
        .value_kind:     global_buffer
      - .actual_access:  write_only
        .address_space:  global
        .offset:         56
        .size:           8
        .value_kind:     global_buffer
    .group_segment_fixed_size: 139264
    .kernarg_segment_align: 8
    .kernarg_segment_size: 64
    .language:       OpenCL C
    .language_version:
      - 2
      - 0
    .max_flat_workgroup_size: 512
    .name:           _Z9nerf_mainPKfS0_S0_PKiS2_PKcS0_Pf
    .private_segment_fixed_size: 0
    .sgpr_count:     55
    .sgpr_spill_count: 0
    .symbol:         _Z9nerf_mainPKfS0_S0_PKiS2_PKcS0_Pf.kd
    .uniform_work_group_size: 1
    .uses_dynamic_stack: false
    .vgpr_count:     256
    .vgpr_spill_count: 0
    .wavefront_size: 64
